# peeled first phase-B block run as two sequential column halves
# speedup vs baseline: 1.0178x; 1.0017x over previous
_Z12fused_kernelPKfS0_Pf:
	s_load_dwordx4 s[12:15], s[0:1], 0x0
	s_load_dwordx2 s[8:9], s[0:1], 0x10
	s_lshl_b32 s0, s2, 5
	s_and_b32 s0, s0, 0xe0
	s_lshr_b32 s3, s2, 3
	s_add_i32 s0, s0, s3
	v_and_b32_e32 v1, 63, v0
	v_lshrrev_b32_e32 v200, 6, v0
	s_lshl_b32 s0, s0, 17
	v_lshlrev_b32_e32 v194, 4, v0
	v_lshl_add_u32 v2, v200, 25, s0
	v_lshlrev_b32_e32 v198, 4, v1
	v_add_u32_e32 v106, 0x2000, v194
	v_add_u32_e32 v107, 0x4000, v194
	v_or_b32_e32 v203, v2, v198
	v_lshlrev_b32_e32 v196, 10, v200
	v_mov_b32_e32 v195, 0
	v_or_b32_e32 v233, v203, v196
	s_mov_b32 s7, 0x20000
	s_brev_b32 s6, 8
	s_waitcnt lgkmcnt(0)
	s_and_b32 s5, s13, 0xffff
	s_mov_b32 s4, s12
	buffer_load_dwordx4 v[70:73], v233, s[4:7], 0 offen nt
	v_or_b32_e32 v227, 0x2000, v233
	buffer_load_dwordx4 v[66:69], v227, s[4:7], 0 offen nt
	v_or_b32_e32 v226, 0x4000, v233
	buffer_load_dwordx4 v[78:81], v226, s[4:7], 0 offen nt
	v_or_b32_e32 v227, 0x6000, v233
	buffer_load_dwordx4 v[74:77], v227, s[4:7], 0 offen nt
	v_or_b32_e32 v226, 0x8000, v233
	buffer_load_dwordx4 v[86:89], v226, s[4:7], 0 offen nt
	v_or_b32_e32 v227, 0xa000, v233
	buffer_load_dwordx4 v[82:85], v227, s[4:7], 0 offen nt
	v_or_b32_e32 v226, 0xc000, v233
	buffer_load_dwordx4 v[94:97], v226, s[4:7], 0 offen nt
	v_or_b32_e32 v227, 0xe000, v233
	buffer_load_dwordx4 v[90:93], v227, s[4:7], 0 offen nt
	v_or_b32_e32 v226, 0x10000, v233
	buffer_load_dwordx4 v[150:153], v226, s[4:7], 0 offen nt
	v_or_b32_e32 v227, 0x12000, v233
	buffer_load_dwordx4 v[146:149], v227, s[4:7], 0 offen nt
	v_or_b32_e32 v226, 0x14000, v233
	buffer_load_dwordx4 v[162:165], v226, s[4:7], 0 offen nt
	v_or_b32_e32 v227, 0x16000, v233
	buffer_load_dwordx4 v[154:157], v227, s[4:7], 0 offen nt
	v_or_b32_e32 v226, 0x18000, v233
	buffer_load_dwordx4 v[174:177], v226, s[4:7], 0 offen nt
	v_or_b32_e32 v227, 0x1a000, v233
	buffer_load_dwordx4 v[166:169], v227, s[4:7], 0 offen nt
	v_or_b32_e32 v226, 0x1c000, v233
	buffer_load_dwordx4 v[182:185], v226, s[4:7], 0 offen nt
	v_or_b32_e32 v227, 0x1e000, v233
	buffer_load_dwordx4 v[178:181], v227, s[4:7], 0 offen nt
	global_load_dwordx4 v[228:231], v194, s[14:15]
	global_load_dwordx4 v[98:101], v106, s[14:15]
	global_load_dwordx4 v[102:105], v107, s[14:15]
	v_add_u32_e32 v107, 0x6000, v194
	global_load_dwordx4 v[116:119], v107, s[14:15]
	v_add_u32_e32 v106, 0x8000, v194
	global_load_dwordx4 v[120:123], v106, s[14:15]
	v_add_u32_e32 v107, 0xa000, v194
	global_load_dwordx4 v[124:127], v107, s[14:15]
	v_add_u32_e32 v106, 0xc000, v194
	global_load_dwordx4 v[128:131], v106, s[14:15]
	v_add_u32_e32 v107, 0xe000, v194
	global_load_dwordx4 v[132:135], v107, s[14:15]
	v_add_u32_e32 v106, 0x10000, v194
	global_load_dwordx4 v[136:139], v106, s[14:15]
	v_add_u32_e32 v107, 0x12000, v194
	global_load_dwordx4 v[140:143], v107, s[14:15]
	v_add_u32_e32 v106, 0x14000, v194
	global_load_dwordx4 v[158:161], v106, s[14:15]
	v_add_u32_e32 v107, 0x16000, v194
	global_load_dwordx4 v[170:173], v107, s[14:15]
	v_add_u32_e32 v106, 0x18000, v194
	global_load_dwordx4 v[186:189], v106, s[14:15]
	v_add_u32_e32 v107, 0x1a000, v194
	global_load_dwordx4 v[190:193], v107, s[14:15]
	v_add_u32_e32 v106, 0x1c000, v194
	global_load_dwordx4 v[204:207], v106, s[14:15]
	v_add_u32_e32 v107, 0x1e000, v194
	global_load_dwordx4 v[208:211], v107, s[14:15]
	v_add_u32_e32 v106, 0x20000, v194
	global_load_dwordx4 v[212:215], v106, s[14:15]
	v_add_u32_e32 v107, 0x22000, v194
	global_load_dwordx4 v[216:219], v107, s[14:15]
	v_add_u32_e32 v106, 0x24000, v194
	global_load_dwordx4 v[220:223], v106, s[14:15]
	v_add_u32_e32 v107, 0x26000, v194
	global_load_dwordx4 v[112:115], v107, s[14:15]
	v_add_u32_e32 v224, 0x400, v196
	s_movk_i32 s0, 0x1c00
	v_and_or_b32 v224, v224, s0, v203
	buffer_load_dwordx4 v[62:65], v224, s[4:7], 0 offen nt
	v_or_b32_e32 v227, 0x2000, v224
	buffer_load_dwordx4 v[38:41], v227, s[4:7], 0 offen nt
	v_or_b32_e32 v226, 0x4000, v224
	buffer_load_dwordx4 v[42:45], v226, s[4:7], 0 offen nt
	v_or_b32_e32 v227, 0x6000, v224
	buffer_load_dwordx4 v[14:17], v227, s[4:7], 0 offen nt
	v_or_b32_e32 v226, 0x8000, v224
	buffer_load_dwordx4 v[46:49], v226, s[4:7], 0 offen nt
	v_or_b32_e32 v227, 0xa000, v224
	buffer_load_dwordx4 v[18:21], v227, s[4:7], 0 offen nt
	v_or_b32_e32 v226, 0xc000, v224
	buffer_load_dwordx4 v[50:53], v226, s[4:7], 0 offen nt
	v_or_b32_e32 v227, 0xe000, v224
	buffer_load_dwordx4 v[22:25], v227, s[4:7], 0 offen nt
	v_or_b32_e32 v226, 0x10000, v224
	buffer_load_dwordx4 v[54:57], v226, s[4:7], 0 offen nt
	v_or_b32_e32 v227, 0x12000, v224
	buffer_load_dwordx4 v[26:29], v227, s[4:7], 0 offen nt
	v_or_b32_e32 v226, 0x14000, v224
	buffer_load_dwordx4 v[58:61], v226, s[4:7], 0 offen nt
	v_or_b32_e32 v227, 0x16000, v224
	buffer_load_dwordx4 v[30:33], v227, s[4:7], 0 offen nt
	v_or_b32_e32 v226, 0x18000, v224
	buffer_load_dwordx4 v[34:37], v226, s[4:7], 0 offen nt
	v_or_b32_e32 v227, 0x1a000, v224
	buffer_load_dwordx4 v[6:9], v227, s[4:7], 0 offen nt
	v_or_b32_e32 v226, 0x1c000, v224
	buffer_load_dwordx4 v[10:13], v226, s[4:7], 0 offen nt
	v_or_b32_e32 v227, 0x1e000, v224
	buffer_load_dwordx4 v[2:5], v227, s[4:7], 0 offen nt
	s_mov_b32 s1, 0xe000
	s_mov_b32 s10, 0xa000
	s_mov_b32 s11, 0x6000
	s_mov_b32 s12, 0xc000
	s_mov_b32 s13, 0x8000
	s_mov_b32 s14, 0x1e000
	s_mov_b32 s15, 0x1c000
	s_mov_b32 s16, 0x2000
	s_mov_b32 s17, 0x4000
	s_mov_b32 s18, 0x10000
	s_mov_b32 s19, 0x1a000
	s_mov_b32 s20, 0x18000
	s_mov_b32 s21, 0x16000
	s_mov_b32 s22, 0x14000
	s_mov_b32 s23, 0x12000
	s_mov_b32 s24, 0xe0
	s_mov_b32 s26, 0x3e13bb63
	v_lshrrev_b32_e32 v144, 3, v0
	v_bfe_u32 v145, v0, 1, 2
	v_lshlrev_b32_e32 v108, 3, v0
	v_and_b32_e32 v109, 8, v108
	v_lshlrev_b32_e32 v224, 8, v144
	v_lshlrev_b32_e32 v225, 6, v145
	v_lshlrev_b32_e32 v226, 8, v145
	v_lshlrev_b32_e32 v110, 10, v144
	v_or3_b32 v110, v226, v110, v109
	v_or3_b32 v111, v224, v225, v109
	v_add_u32_e32 v111, 0xff00, v111
	v_add_u32_e32 v144, 0x24800, v194
	v_bfe_u32 v201, v0, 4, 2
	v_and_b32_e32 v197, 15, v0
	v_lshlrev_b32_e32 v202, 2, v201
	s_waitcnt vmcnt(34)
	v_pk_add_f32 v[224:225], v[228:229], 0 op_sel_hi:[1,0]
	v_pk_add_f32 v[226:227], v[230:231], 0 op_sel_hi:[1,0]
	v_cvt_pk_bf16_f32 v228, v228, v229
	v_cvt_pk_bf16_f32 v229, v230, v231
	v_pk_add_f32 v[224:225], v[224:225], v[98:99]
	v_pk_add_f32 v[226:227], v[226:227], v[100:101]
	v_cvt_pk_bf16_f32 v98, v98, v99
	v_cvt_pk_bf16_f32 v99, v100, v101
	ds_write2_b64 v110, v[228:229], v[98:99] offset1:2
	s_waitcnt vmcnt(32)
	v_pk_add_f32 v[224:225], v[224:225], v[102:103]
	v_pk_add_f32 v[226:227], v[226:227], v[104:105]
	v_cvt_pk_bf16_f32 v102, v102, v103
	v_cvt_pk_bf16_f32 v103, v104, v105
	v_pk_add_f32 v[224:225], v[224:225], v[116:117]
	v_pk_add_f32 v[226:227], v[226:227], v[118:119]
	v_cvt_pk_bf16_f32 v116, v116, v117
	v_cvt_pk_bf16_f32 v117, v118, v119
	ds_write2_b64 v110, v[102:103], v[116:117] offset0:4 offset1:6
	s_waitcnt vmcnt(30)
	v_pk_add_f32 v[224:225], v[224:225], v[120:121]
	v_pk_add_f32 v[226:227], v[226:227], v[122:123]
	v_cvt_pk_bf16_f32 v120, v120, v121
	v_cvt_pk_bf16_f32 v121, v122, v123
	v_pk_add_f32 v[224:225], v[224:225], v[124:125]
	v_pk_add_f32 v[226:227], v[226:227], v[126:127]
	v_cvt_pk_bf16_f32 v124, v124, v125
	v_cvt_pk_bf16_f32 v125, v126, v127
	ds_write2_b64 v110, v[120:121], v[124:125] offset0:8 offset1:10
	s_waitcnt vmcnt(28)
	v_pk_add_f32 v[224:225], v[224:225], v[128:129]
	v_pk_add_f32 v[226:227], v[226:227], v[130:131]
	v_cvt_pk_bf16_f32 v128, v128, v129
	v_cvt_pk_bf16_f32 v129, v130, v131
	v_pk_add_f32 v[224:225], v[224:225], v[132:133]
	v_pk_add_f32 v[226:227], v[226:227], v[134:135]
	v_cvt_pk_bf16_f32 v132, v132, v133
	v_cvt_pk_bf16_f32 v133, v134, v135
	ds_write2_b64 v110, v[128:129], v[132:133] offset0:12 offset1:14
	s_waitcnt vmcnt(26)
	v_pk_add_f32 v[224:225], v[224:225], v[136:137]
	v_pk_add_f32 v[226:227], v[226:227], v[138:139]
	v_cvt_pk_bf16_f32 v136, v136, v137
	v_cvt_pk_bf16_f32 v137, v138, v139
	v_pk_add_f32 v[224:225], v[224:225], v[140:141]
	v_pk_add_f32 v[226:227], v[226:227], v[142:143]
	v_cvt_pk_bf16_f32 v140, v140, v141
	v_cvt_pk_bf16_f32 v141, v142, v143
	ds_write2_b64 v110, v[136:137], v[140:141] offset0:16 offset1:18
	s_waitcnt vmcnt(24)
	v_pk_add_f32 v[224:225], v[224:225], v[158:159]
	v_pk_add_f32 v[226:227], v[226:227], v[160:161]
	v_cvt_pk_bf16_f32 v158, v158, v159
	v_cvt_pk_bf16_f32 v159, v160, v161
	v_pk_add_f32 v[224:225], v[224:225], v[170:171]
	v_pk_add_f32 v[226:227], v[226:227], v[172:173]
	v_cvt_pk_bf16_f32 v170, v170, v171
	v_cvt_pk_bf16_f32 v171, v172, v173
	ds_write2_b64 v110, v[158:159], v[170:171] offset0:20 offset1:22
	s_waitcnt vmcnt(22)
	v_pk_add_f32 v[224:225], v[224:225], v[186:187]
	v_pk_add_f32 v[226:227], v[226:227], v[188:189]
	v_cvt_pk_bf16_f32 v186, v186, v187
	v_cvt_pk_bf16_f32 v187, v188, v189
	v_pk_add_f32 v[224:225], v[224:225], v[190:191]
	v_pk_add_f32 v[226:227], v[226:227], v[192:193]
	v_cvt_pk_bf16_f32 v190, v190, v191
	v_cvt_pk_bf16_f32 v191, v192, v193
	ds_write2_b64 v110, v[186:187], v[190:191] offset0:24 offset1:26
	s_waitcnt vmcnt(20)
	v_pk_add_f32 v[224:225], v[224:225], v[204:205]
	v_pk_add_f32 v[226:227], v[226:227], v[206:207]
	v_cvt_pk_bf16_f32 v204, v204, v205
	v_cvt_pk_bf16_f32 v205, v206, v207
	v_pk_add_f32 v[224:225], v[224:225], v[208:209]
	v_pk_add_f32 v[226:227], v[226:227], v[210:211]
	v_cvt_pk_bf16_f32 v208, v208, v209
	v_cvt_pk_bf16_f32 v209, v210, v211
	ds_write2_b64 v110, v[204:205], v[208:209] offset0:28 offset1:30
	s_waitcnt vmcnt(18)
	v_pk_add_f32 v[224:225], v[224:225], v[212:213]
	v_pk_add_f32 v[226:227], v[226:227], v[214:215]
	v_cvt_pk_bf16_f32 v212, v212, v213
	v_cvt_pk_bf16_f32 v213, v214, v215
	v_pk_add_f32 v[224:225], v[224:225], v[216:217]
	v_pk_add_f32 v[226:227], v[226:227], v[218:219]
	v_cvt_pk_bf16_f32 v216, v216, v217
	v_cvt_pk_bf16_f32 v217, v218, v219
	ds_write2_b64 v111, v[212:213], v[216:217] offset0:32 offset1:34
	s_waitcnt vmcnt(16)
	v_pk_add_f32 v[224:225], v[224:225], v[220:221]
	v_pk_add_f32 v[226:227], v[226:227], v[222:223]
	v_cvt_pk_bf16_f32 v220, v220, v221
	v_cvt_pk_bf16_f32 v221, v222, v223
	v_pk_add_f32 v[224:225], v[224:225], v[112:113]
	v_pk_add_f32 v[226:227], v[226:227], v[114:115]
	v_cvt_pk_bf16_f32 v112, v112, v113
	v_cvt_pk_bf16_f32 v113, v114, v115
	ds_write2_b64 v111, v[220:221], v[112:113] offset0:36 offset1:38
	v_pk_mul_f32 v[224:225], v[224:225], s[26:27] op_sel_hi:[1,0]
	v_pk_mul_f32 v[226:227], v[226:227], s[26:27] op_sel_hi:[1,0]
	ds_write_b128 v144, v[224:227]
	v_and_or_b32 v98, v0, 3, v202
	v_mov_b32_e32 v99, 0x10000
	v_lshl_or_b32 v204, v98, 4, v99
	s_movk_i32 s25, 0x2100
	v_mov_b32_e32 v98, 0x14000
	v_mad_u32_u24 v199, v200, s25, v98
	v_add_u32_e32 v98, 0x800, v196
	v_and_or_b32 v186, v98, s0, v203
	v_or_b32_e32 v98, 0x2000, v186
	s_waitcnt lgkmcnt(0)
	s_barrier
	buffer_load_dwordx4 v[102:105], v186, s[4:7], 0 offen nt
	s_nop 0
	buffer_load_dwordx4 v[98:101], v98, s[4:7], 0 offen nt
	v_or_b32_e32 v106, 0x4000, v186
	v_or_b32_e32 v107, 0x6000, v186
	v_or_b32_e32 v114, 0x8000, v186
	v_or_b32_e32 v115, 0xa000, v186
	v_or_b32_e32 v122, 0xc000, v186
	v_or_b32_e32 v123, 0xe000, v186
	v_or_b32_e32 v130, 0x10000, v186
	v_or_b32_e32 v131, 0x12000, v186
	v_or_b32_e32 v138, 0x14000, v186
	v_or_b32_e32 v139, 0x16000, v186
	v_or_b32_e32 v158, 0x18000, v186
	v_or_b32_e32 v159, 0x1a000, v186
	v_or_b32_e32 v187, 0x1c000, v186
	v_or_b32_e32 v186, 0x1e000, v186
	v_or_b32_e32 v213, v199, v109
	v_and_b32_e32 v214, 0x1f0, v108
	buffer_load_dwordx4 v[110:113], v106, s[4:7], 0 offen nt
	s_nop 0
	buffer_load_dwordx4 v[106:109], v107, s[4:7], 0 offen nt
	s_nop 0
	buffer_load_dwordx4 v[118:121], v114, s[4:7], 0 offen nt
	s_nop 0
	buffer_load_dwordx4 v[114:117], v115, s[4:7], 0 offen nt
	s_nop 0
	buffer_load_dwordx4 v[126:129], v122, s[4:7], 0 offen nt
	s_nop 0
	buffer_load_dwordx4 v[122:125], v123, s[4:7], 0 offen nt
	s_nop 0
	buffer_load_dwordx4 v[134:137], v130, s[4:7], 0 offen nt
	s_nop 0
	buffer_load_dwordx4 v[130:133], v131, s[4:7], 0 offen nt
	s_nop 0
	buffer_load_dwordx4 v[142:145], v138, s[4:7], 0 offen nt
	s_nop 0
	buffer_load_dwordx4 v[138:141], v139, s[4:7], 0 offen nt
	s_nop 0
	buffer_load_dwordx4 v[170:173], v158, s[4:7], 0 offen nt
	s_nop 0
	buffer_load_dwordx4 v[158:161], v159, s[4:7], 0 offen nt
	s_nop 0
	buffer_load_dwordx4 v[190:193], v187, s[4:7], 0 offen nt
	s_nop 0
	buffer_load_dwordx4 v[186:189], v186, s[4:7], 0 offen nt
	s_waitcnt vmcnt(32)
	v_cvt_pk_bf16_f32 v66, v66, v67
	v_cvt_pk_bf16_f32 v67, v68, v69
	s_movk_i32 s25, 0x50
	v_xad_u32 v207, v214, s25, v213
	s_movk_i32 s25, 0x60
	v_xad_u32 v206, v214, s25, v213
	s_movk_i32 s25, 0x70
	v_xad_u32 v205, v214, s25, v213
	s_movk_i32 s25, 0x80
	v_xad_u32 v211, v214, 16, v213
	v_xad_u32 v231, v214, s25, v213
	s_movk_i32 s25, 0x90
	v_xad_u32 v210, v214, 32, v213
	v_xad_u32 v230, v214, s25, v213
	s_movk_i32 s25, 0xa0
	ds_write_b64 v211, v[66:67] offset:512
	v_cvt_pk_bf16_f32 v66, v78, v79
	v_cvt_pk_bf16_f32 v67, v80, v81
	v_xad_u32 v209, v214, 48, v213
	v_xad_u32 v229, v214, s25, v213
	s_movk_i32 s25, 0xb0
	ds_write_b64 v210, v[66:67] offset:1024
	v_cvt_pk_bf16_f32 v66, v74, v75
	v_cvt_pk_bf16_f32 v67, v76, v77
	v_xad_u32 v208, v214, 64, v213
	v_xad_u32 v228, v214, s25, v213
	s_movk_i32 s25, 0xc0
	ds_write_b64 v209, v[66:67] offset:1536
	v_cvt_pk_bf16_f32 v66, v86, v87
	v_cvt_pk_bf16_f32 v67, v88, v89
	v_xad_u32 v227, v214, s25, v213
	s_movk_i32 s25, 0xd0
	v_xad_u32 v225, v214, s24, v213
	s_movk_i32 s24, 0xf0
	ds_write_b64 v208, v[66:67] offset:2048
	v_cvt_pk_bf16_f32 v66, v82, v83
	v_cvt_pk_bf16_f32 v67, v84, v85
	v_add_u32_e32 v212, v213, v214
	v_xad_u32 v226, v214, s25, v213
	v_xad_u32 v224, v214, s24, v213
	v_lshl_add_u32 v213, v197, 9, v199
	v_bitop3_b32 v214, v201, v0, 15 bitop3:0x78
	ds_write_b64 v207, v[66:67] offset:2560
	v_cvt_pk_bf16_f32 v66, v94, v95
	v_cvt_pk_bf16_f32 v67, v96, v97
	v_lshl_or_b32 v223, v214, 4, v213
	v_bitop3_b32 v214, v201, v197, 4 bitop3:0x36
	ds_write_b64 v206, v[66:67] offset:3072
	v_cvt_pk_bf16_f32 v66, v90, v91
	v_cvt_pk_bf16_f32 v67, v92, v93
	v_lshl_or_b32 v222, v214, 4, v213
	v_bitop3_b32 v214, v201, v197, 8 bitop3:0x36
	ds_write_b64 v205, v[66:67] offset:3584
	v_cvt_pk_bf16_f32 v66, v150, v151
	v_cvt_pk_bf16_f32 v67, v152, v153
	v_lshl_or_b32 v221, v214, 4, v213
	v_bitop3_b32 v214, v201, v197, 12 bitop3:0x36
	ds_write_b64 v231, v[66:67] offset:4096
	v_cvt_pk_bf16_f32 v66, v146, v147
	v_cvt_pk_bf16_f32 v67, v148, v149
	v_lshl_or_b32 v219, v214, 4, v213
	v_bitop3_b32 v214, v201, v197, 16 bitop3:0x36
	ds_write_b64 v230, v[66:67] offset:4608
	v_cvt_pk_bf16_f32 v66, v162, v163
	v_cvt_pk_bf16_f32 v67, v164, v165
	v_lshl_add_u32 v218, v214, 4, v213
	v_bitop3_b32 v214, v201, v197, 20 bitop3:0x36
	ds_write_b64 v229, v[66:67] offset:5120
	v_cvt_pk_bf16_f32 v66, v154, v155
	v_cvt_pk_bf16_f32 v67, v156, v157
	v_lshl_add_u32 v217, v214, 4, v213
	v_bitop3_b32 v214, v201, v197, 24 bitop3:0x36
	ds_write_b64 v228, v[66:67] offset:5632
	v_cvt_pk_bf16_f32 v66, v174, v175
	v_cvt_pk_bf16_f32 v67, v176, v177
	v_lshl_add_u32 v216, v214, 4, v213
	v_bitop3_b32 v214, v201, v197, 28 bitop3:0x36
	ds_write_b64 v227, v[66:67] offset:6144
	v_cvt_pk_bf16_f32 v66, v166, v167
	v_cvt_pk_bf16_f32 v67, v168, v169
	v_add_u32_e32 v235, 3, v200
	v_lshl_add_u32 v213, v214, 4, v213
	ds_write_b64 v226, v[66:67] offset:6656
	v_cvt_pk_bf16_f32 v66, v182, v183
	v_cvt_pk_bf16_f32 v67, v184, v185
	v_cvt_pk_bf16_f32 v70, v70, v71
	v_cvt_pk_bf16_f32 v71, v72, v73
	ds_write_b64 v212, v[70:71]
	ds_write_b64 v225, v[66:67] offset:7168
	v_cvt_pk_bf16_f32 v66, v178, v179
	v_cvt_pk_bf16_f32 v67, v180, v181
	ds_write_b64 v224, v[66:67] offset:7680
	v_lshl_or_b32 v66, v200, 13, v198
	ds_read_b128 v[66:69], v66
	v_lshlrev_b32_e32 v220, 11, v200
	v_or_b32_e32 v70, v204, v220
	ds_read_b128 v[70:73], v70
	ds_read_b128 v[74:77], v223
	v_lshlrev_b32_e32 v232, 3, v200
	v_or_b32_e32 v214, 1, v232
	s_waitcnt lgkmcnt(0)
	v_mfma_f32_16x16x32_bf16 v[70:73], v[70:73], v[74:77], 0
	v_lshlrev_b32_e32 v215, 8, v214
	v_or_b32_e32 v78, v204, v215
	v_or_b32_e32 v184, 2, v232
	v_mfma_f32_16x16x32_bf16 v[66:69], v[66:69], v[74:77], 0
	v_lshl_or_b32 v74, v214, 10, v198
	ds_read_b128 v[74:77], v74
	ds_read_b128 v[78:81], v78
	ds_read_b128 v[82:85], v222
	v_lshlrev_b32_e32 v185, 8, v184
	s_waitcnt lgkmcnt(0)
	v_mfma_f32_16x16x32_bf16 v[70:73], v[78:81], v[82:85], v[70:73]
	v_or_b32_e32 v78, v204, v185
	v_or_b32_e32 v182, 3, v232
	v_lshlrev_b32_e32 v183, 8, v182
	v_mfma_f32_16x16x32_bf16 v[66:69], v[74:77], v[82:85], v[66:69]
	v_lshl_or_b32 v74, v184, 10, v198
	ds_read_b128 v[74:77], v74
	ds_read_b128 v[78:81], v78
	ds_read_b128 v[82:85], v221
	s_waitcnt lgkmcnt(0)
	v_mfma_f32_16x16x32_bf16 v[70:73], v[78:81], v[82:85], v[70:73]
	v_or_b32_e32 v78, v204, v183
	v_or_b32_e32 v180, 4, v232
	v_lshlrev_b32_e32 v181, 8, v180
	v_mfma_f32_16x16x32_bf16 v[66:69], v[74:77], v[82:85], v[66:69]
	v_lshl_or_b32 v74, v182, 10, v198
	ds_read_b128 v[74:77], v74
	ds_read_b128 v[78:81], v78
	ds_read_b128 v[82:85], v219
	s_waitcnt lgkmcnt(0)
	v_mfma_f32_16x16x32_bf16 v[66:69], v[74:77], v[82:85], v[66:69]
	v_lshl_or_b32 v74, v180, 10, v198
	ds_read_b128 v[74:77], v74
	v_or_b32_e32 v178, 5, v232
	v_mfma_f32_16x16x32_bf16 v[70:73], v[78:81], v[82:85], v[70:73]
	v_or_b32_e32 v78, v204, v181
	ds_read_b128 v[78:81], v78
	ds_read_b128 v[82:85], v218
	v_lshlrev_b32_e32 v179, 8, v178
	s_waitcnt lgkmcnt(0)
	v_mfma_f32_16x16x32_bf16 v[66:69], v[74:77], v[82:85], v[66:69]
	v_lshl_or_b32 v74, v178, 10, v198
	ds_read_b128 v[74:77], v74
	v_or_b32_e32 v176, 6, v232
	v_mfma_f32_16x16x32_bf16 v[70:73], v[78:81], v[82:85], v[70:73]
	v_or_b32_e32 v78, v204, v179
	ds_read_b128 v[78:81], v78
	ds_read_b128 v[82:85], v217
	v_lshlrev_b32_e32 v177, 8, v176
	s_waitcnt lgkmcnt(0)
	v_mfma_f32_16x16x32_bf16 v[66:69], v[74:77], v[82:85], v[66:69]
	v_lshl_or_b32 v74, v176, 10, v198
	ds_read_b128 v[74:77], v74
	v_or_b32_e32 v174, 7, v232
	v_mfma_f32_16x16x32_bf16 v[70:73], v[78:81], v[82:85], v[70:73]
	v_or_b32_e32 v78, v204, v177
	ds_read_b128 v[78:81], v78
	ds_read_b128 v[82:85], v216
	v_lshlrev_b32_e32 v175, 8, v174
	s_waitcnt lgkmcnt(0)
	v_mfma_f32_16x16x32_bf16 v[66:69], v[74:77], v[82:85], v[66:69]
	v_lshl_or_b32 v74, v174, 10, v198
	s_waitcnt vmcnt(16)
	v_cvt_pk_bf16_f32 v14, v14, v15
	v_cvt_pk_bf16_f32 v15, v16, v17
	v_mfma_f32_16x16x32_bf16 v[70:73], v[78:81], v[82:85], v[70:73]
	v_or_b32_e32 v78, v204, v175
	ds_read_b128 v[74:77], v74
	ds_read_b128 v[78:81], v78
	ds_read_b128 v[82:85], v213
	ds_write_b64 v209, v[14:15] offset:1536
	v_cvt_pk_bf16_f32 v14, v46, v47
	v_cvt_pk_bf16_f32 v15, v48, v49
	ds_write_b64 v208, v[14:15] offset:2048
	v_cvt_pk_bf16_f32 v14, v18, v19
	v_cvt_pk_bf16_f32 v15, v20, v21
	ds_write_b64 v207, v[14:15] offset:2560
	v_cvt_pk_bf16_f32 v14, v50, v51
	v_cvt_pk_bf16_f32 v15, v52, v53
	ds_write_b64 v206, v[14:15] offset:3072
	v_cvt_pk_bf16_f32 v14, v22, v23
	v_cvt_pk_bf16_f32 v15, v24, v25
	ds_write_b64 v205, v[14:15] offset:3584
	v_cvt_pk_bf16_f32 v14, v54, v55
	v_cvt_pk_bf16_f32 v15, v56, v57
	v_cvt_pk_bf16_f32 v6, v6, v7
	v_cvt_pk_bf16_f32 v2, v2, v3
	ds_write_b64 v231, v[14:15] offset:4096
	v_cvt_pk_bf16_f32 v14, v26, v27
	v_cvt_pk_bf16_f32 v15, v28, v29
	v_cvt_pk_bf16_f32 v7, v8, v9
	ds_write_b64 v226, v[6:7] offset:6656
	v_cvt_pk_bf16_f32 v6, v10, v11
	v_cvt_pk_bf16_f32 v3, v4, v5
	ds_write_b64 v224, v[2:3] offset:7680
	v_lshlrev_b32_e32 v2, 10, v235
	ds_write_b64 v230, v[14:15] offset:4608
	v_cvt_pk_bf16_f32 v14, v58, v59
	v_cvt_pk_bf16_f32 v15, v60, v61
	v_cvt_pk_bf16_f32 v7, v12, v13
	ds_write_b64 v225, v[6:7] offset:7168
	v_and_or_b32 v6, v2, s0, v203
	ds_write_b64 v229, v[14:15] offset:5120
	v_cvt_pk_bf16_f32 v14, v30, v31
	v_cvt_pk_bf16_f32 v15, v32, v33
	v_or_b32_e32 v7, 0x2000, v6
	ds_write_b64 v228, v[14:15] offset:5632
	v_cvt_pk_bf16_f32 v14, v34, v35
	v_cvt_pk_bf16_f32 v15, v36, v37
	buffer_load_dwordx4 v[2:5], v6, s[4:7], 0 offen nt
	buffer_load_dwordx4 v[10:13], v7, s[4:7], 0 offen nt
	v_or_b32_e32 v7, 0x4000, v6
	ds_write_b64 v227, v[14:15] offset:6144
	buffer_load_dwordx4 v[14:17], v7, s[4:7], 0 offen nt
	v_or_b32_e32 v7, 0x6000, v6
	v_cvt_pk_bf16_f32 v38, v38, v39
	v_cvt_pk_bf16_f32 v39, v40, v41
	buffer_load_dwordx4 v[22:25], v7, s[4:7], 0 offen nt
	v_or_b32_e32 v7, 0x8000, v6
	ds_write_b64 v211, v[38:39] offset:512
	v_cvt_pk_bf16_f32 v38, v42, v43
	v_cvt_pk_bf16_f32 v39, v44, v45
	buffer_load_dwordx4 v[30:33], v7, s[4:7], 0 offen nt
	v_or_b32_e32 v7, 0xa000, v6
	ds_write_b64 v210, v[38:39] offset:1024
	buffer_load_dwordx4 v[38:41], v7, s[4:7], 0 offen nt
	v_or_b32_e32 v7, 0xc000, v6
	buffer_load_dwordx4 v[46:49], v7, s[4:7], 0 offen nt
	v_or_b32_e32 v7, 0xe000, v6
	v_cvt_pk_bf16_f32 v62, v62, v63
	v_cvt_pk_bf16_f32 v63, v64, v65
	buffer_load_dwordx4 v[54:57], v7, s[4:7], 0 offen nt
	v_or_b32_e32 v7, 0x10000, v6
	ds_write_b64 v212, v[62:63]
	buffer_load_dwordx4 v[62:65], v7, s[4:7], 0 offen nt
	v_or_b32_e32 v7, 0x12000, v6
	s_waitcnt lgkmcnt(14)
	v_mfma_f32_16x16x32_bf16 v[66:69], v[74:77], v[82:85], v[66:69]
	v_mfma_f32_16x16x32_bf16 v[74:77], v[78:81], v[82:85], v[70:73]
	s_nop 2
	buffer_load_dwordx4 v[70:73], v7, s[4:7], 0 offen nt
	v_or_b32_e32 v7, 0x14000, v6
	buffer_load_dwordx4 v[78:81], v7, s[4:7], 0 offen nt
	v_or_b32_e32 v7, 0x16000, v6
	buffer_load_dwordx4 v[86:89], v7, s[4:7], 0 offen nt
	v_or_b32_e32 v7, 0x18000, v6
	buffer_load_dwordx4 v[94:97], v7, s[4:7], 0 offen nt
	v_or_b32_e32 v7, 0x1a000, v6
	buffer_load_dwordx4 v[146:149], v7, s[4:7], 0 offen nt
	v_or_b32_e32 v7, 0x1c000, v6
	v_or_b32_e32 v6, 0x1e000, v6
	buffer_load_dwordx4 v[150:153], v7, s[4:7], 0 offen nt
	buffer_load_dwordx4 v[154:157], v6, s[4:7], 0 offen nt
	v_add_u32_e32 v6, 8, v232
	v_and_b32_e32 v50, 56, v6
	v_lshl_or_b32 v6, v50, 10, v198
	ds_read_b128 v[6:9], v6
	v_lshl_or_b32 v18, v50, 8, v204
	ds_read_b128 v[18:21], v18
	ds_read_b128 v[26:29], v223
	v_or_b32_e32 v34, 1, v50
	s_movk_i32 s24, 0x1000
	s_waitcnt lgkmcnt(0)
	v_mfma_f32_16x16x32_bf16 v[18:21], v[18:21], v[26:29], v[74:77]
	v_add_u32_e32 v234, 5, v200
	v_mfma_f32_16x16x32_bf16 v[6:9], v[6:9], v[26:29], v[66:69]
	v_lshl_or_b32 v26, v34, 10, v198
	ds_read_b128 v[26:29], v26
	v_lshl_or_b32 v34, v34, 8, v204
	ds_read_b128 v[34:37], v34
	ds_read_b128 v[42:45], v222
	s_waitcnt lgkmcnt(0)
	v_mfma_f32_16x16x32_bf16 v[18:21], v[34:37], v[42:45], v[18:21]
	v_or_b32_e32 v34, 2, v50
	v_mfma_f32_16x16x32_bf16 v[6:9], v[26:29], v[42:45], v[6:9]
	v_lshl_or_b32 v26, v34, 10, v198
	ds_read_b128 v[26:29], v26
	v_lshl_or_b32 v34, v34, 8, v204
	ds_read_b128 v[34:37], v34
	ds_read_b128 v[42:45], v221
	s_waitcnt lgkmcnt(0)
	v_mfma_f32_16x16x32_bf16 v[18:21], v[34:37], v[42:45], v[18:21]
	v_or_b32_e32 v34, 3, v50
	v_mfma_f32_16x16x32_bf16 v[6:9], v[26:29], v[42:45], v[6:9]
	v_lshl_or_b32 v26, v34, 10, v198
	ds_read_b128 v[26:29], v26
	v_lshl_or_b32 v34, v34, 8, v204
	ds_read_b128 v[34:37], v34
	ds_read_b128 v[42:45], v219
	s_waitcnt lgkmcnt(0)
	v_mfma_f32_16x16x32_bf16 v[18:21], v[34:37], v[42:45], v[18:21]
	v_or_b32_e32 v34, 4, v50
	v_mfma_f32_16x16x32_bf16 v[6:9], v[26:29], v[42:45], v[6:9]
	v_lshl_or_b32 v26, v34, 10, v198
	ds_read_b128 v[26:29], v26
	v_lshl_or_b32 v34, v34, 8, v204
	ds_read_b128 v[34:37], v34
	ds_read_b128 v[42:45], v218
	s_waitcnt lgkmcnt(0)
	v_mfma_f32_16x16x32_bf16 v[18:21], v[34:37], v[42:45], v[18:21]
	v_or_b32_e32 v34, 5, v50
	v_mfma_f32_16x16x32_bf16 v[6:9], v[26:29], v[42:45], v[6:9]
	v_lshl_or_b32 v26, v34, 10, v198
	ds_read_b128 v[26:29], v26
	v_lshl_or_b32 v34, v34, 8, v204
	ds_read_b128 v[34:37], v34
	ds_read_b128 v[42:45], v217
	s_waitcnt lgkmcnt(0)
	v_mfma_f32_16x16x32_bf16 v[18:21], v[34:37], v[42:45], v[18:21]
	v_or_b32_e32 v34, 6, v50
	v_mfma_f32_16x16x32_bf16 v[6:9], v[26:29], v[42:45], v[6:9]
	v_lshl_or_b32 v26, v34, 10, v198
	ds_read_b128 v[26:29], v26
	v_lshl_or_b32 v34, v34, 8, v204
	ds_read_b128 v[34:37], v34
	ds_read_b128 v[42:45], v216
	s_waitcnt lgkmcnt(0)
	v_mfma_f32_16x16x32_bf16 v[18:21], v[34:37], v[42:45], v[18:21]
	v_or_b32_e32 v34, 7, v50
	v_mfma_f32_16x16x32_bf16 v[6:9], v[26:29], v[42:45], v[6:9]
	v_lshl_or_b32 v26, v34, 10, v198
	ds_read_b128 v[26:29], v26
	v_lshl_or_b32 v34, v34, 8, v204
	ds_read_b128 v[34:37], v34
	ds_read_b128 v[42:45], v213
	s_waitcnt lgkmcnt(0)
	v_mfma_f32_16x16x32_bf16 v[162:165], v[26:29], v[42:45], v[6:9]
	s_waitcnt vmcnt(31)
	s_nop 1
	v_cvt_pk_bf16_f32 v6, v102, v103
	v_cvt_pk_bf16_f32 v7, v104, v105
	ds_write_b64 v212, v[6:7]
	s_waitcnt vmcnt(30)
	v_cvt_pk_bf16_f32 v6, v98, v99
	v_cvt_pk_bf16_f32 v7, v100, v101
	ds_write_b64 v211, v[6:7] offset:512
	s_waitcnt vmcnt(29)
	v_cvt_pk_bf16_f32 v6, v110, v111
	v_cvt_pk_bf16_f32 v7, v112, v113
	ds_write_b64 v210, v[6:7] offset:1024
	s_waitcnt vmcnt(28)
	v_cvt_pk_bf16_f32 v6, v106, v107
	v_cvt_pk_bf16_f32 v7, v108, v109
	ds_write_b64 v209, v[6:7] offset:1536
	s_waitcnt vmcnt(27)
	v_cvt_pk_bf16_f32 v6, v118, v119
	v_cvt_pk_bf16_f32 v7, v120, v121
	ds_write_b64 v208, v[6:7] offset:2048
	s_waitcnt vmcnt(26)
	v_cvt_pk_bf16_f32 v6, v114, v115
	v_cvt_pk_bf16_f32 v7, v116, v117
	ds_write_b64 v207, v[6:7] offset:2560
	s_waitcnt vmcnt(25)
	v_cvt_pk_bf16_f32 v6, v126, v127
	v_cvt_pk_bf16_f32 v7, v128, v129
	ds_write_b64 v206, v[6:7] offset:3072
	s_waitcnt vmcnt(24)
	v_cvt_pk_bf16_f32 v6, v122, v123
	v_cvt_pk_bf16_f32 v7, v124, v125
	ds_write_b64 v205, v[6:7] offset:3584
	s_waitcnt vmcnt(23)
	v_cvt_pk_bf16_f32 v6, v134, v135
	v_cvt_pk_bf16_f32 v7, v136, v137
	ds_write_b64 v231, v[6:7] offset:4096
	s_waitcnt vmcnt(22)
	v_cvt_pk_bf16_f32 v6, v130, v131
	v_cvt_pk_bf16_f32 v7, v132, v133
	ds_write_b64 v230, v[6:7] offset:4608
	s_waitcnt vmcnt(21)
	v_cvt_pk_bf16_f32 v6, v142, v143
	v_cvt_pk_bf16_f32 v7, v144, v145
	ds_write_b64 v229, v[6:7] offset:5120
	s_waitcnt vmcnt(20)
	v_cvt_pk_bf16_f32 v6, v138, v139
	v_cvt_pk_bf16_f32 v7, v140, v141
	ds_write_b64 v228, v[6:7] offset:5632
	s_waitcnt vmcnt(19)
	v_cvt_pk_bf16_f32 v6, v170, v171
	v_cvt_pk_bf16_f32 v7, v172, v173
	ds_write_b64 v227, v[6:7] offset:6144
	s_waitcnt vmcnt(18)
	v_cvt_pk_bf16_f32 v6, v158, v159
	v_mov_b32_e32 v106, 0x1000
	v_cvt_pk_bf16_f32 v7, v160, v161
	ds_write_b64 v226, v[6:7] offset:6656
	s_waitcnt vmcnt(17)
	v_cvt_pk_bf16_f32 v6, v190, v191
	v_bitop3_b32 v107, v233, s19, v106 bitop3:0xde
	v_mfma_f32_16x16x32_bf16 v[166:169], v[34:37], v[42:45], v[18:21]
	v_cvt_pk_bf16_f32 v7, v192, v193
	ds_write_b64 v225, v[6:7] offset:7168
	s_waitcnt vmcnt(16)
	v_cvt_pk_bf16_f32 v6, v186, v187
	v_bitop3_b32 v26, v233, s17, v106 bitop3:0xde
	v_bitop3_b32 v34, v233, s11, v106 bitop3:0xde
	v_bitop3_b32 v18, v233, s16, v106 bitop3:0xde
	v_bitop3_b32 v42, v233, s13, v106 bitop3:0xde
	v_bitop3_b32 v50, v233, s10, v106 bitop3:0xde
	v_bitop3_b32 v58, v233, s12, v106 bitop3:0xde
	v_bitop3_b32 v66, v233, s1, v106 bitop3:0xde
	v_bitop3_b32 v74, v233, s18, v106 bitop3:0xde
	v_bitop3_b32 v82, v233, s23, v106 bitop3:0xde
	v_bitop3_b32 v90, v233, s22, v106 bitop3:0xde
	v_bitop3_b32 v98, v233, s21, v106 bitop3:0xde
	v_bitop3_b32 v102, v233, s20, v106 bitop3:0xde
	buffer_load_dwordx4 v[110:113], v107, s[4:7], 0 offen nt
	v_bitop3_b32 v107, v233, s15, v106 bitop3:0xde
	v_bitop3_b32 v106, v233, s14, v106 bitop3:0xde
	v_cvt_pk_bf16_f32 v7, v188, v189
	ds_write_b64 v224, v[6:7] offset:7680
	v_bitop3_b32 v6, v203, s24, v196 bitop3:0x36
	buffer_load_dwordx4 v[42:45], v42, s[4:7], 0 offen nt
	s_nop 0
	buffer_load_dwordx4 v[50:53], v50, s[4:7], 0 offen nt
	s_nop 0
	buffer_load_dwordx4 v[58:61], v58, s[4:7], 0 offen nt
	s_nop 0
	buffer_load_dwordx4 v[66:69], v66, s[4:7], 0 offen nt
	s_nop 0
	buffer_load_dwordx4 v[74:77], v74, s[4:7], 0 offen nt
	s_nop 0
	buffer_load_dwordx4 v[82:85], v82, s[4:7], 0 offen nt
	s_nop 0
	buffer_load_dwordx4 v[90:93], v90, s[4:7], 0 offen nt
	s_nop 0
	buffer_load_dwordx4 v[98:101], v98, s[4:7], 0 offen nt
	s_nop 0
	buffer_load_dwordx4 v[102:105], v102, s[4:7], 0 offen nt
	s_nop 0
	buffer_load_dwordx4 v[126:129], v106, s[4:7], 0 offen nt
	buffer_load_dwordx4 v[118:121], v107, s[4:7], 0 offen nt
	s_nop 0
	buffer_load_dwordx4 v[6:9], v6, s[4:7], 0 offen nt
	s_nop 0
	buffer_load_dwordx4 v[18:21], v18, s[4:7], 0 offen nt
	s_nop 0
	buffer_load_dwordx4 v[26:29], v26, s[4:7], 0 offen nt
	s_nop 0
	buffer_load_dwordx4 v[34:37], v34, s[4:7], 0 offen nt
	v_add_u32_e32 v106, 16, v232
	v_and_b32_e32 v138, 56, v106
	v_lshl_or_b32 v106, v138, 10, v198
	ds_read_b128 v[106:109], v106
	v_lshl_or_b32 v114, v138, 8, v204
	ds_read_b128 v[114:117], v114
	ds_read_b128 v[122:125], v223
	v_or_b32_e32 v130, 1, v138
	s_waitcnt vmcnt(31)
	v_cvt_pk_bf16_f32 v2, v2, v3
	s_waitcnt lgkmcnt(0)
	v_mfma_f32_16x16x32_bf16 v[114:117], v[114:117], v[122:125], v[166:169]
	v_cvt_pk_bf16_f32 v3, v4, v5
	v_mfma_f32_16x16x32_bf16 v[106:109], v[106:109], v[122:125], v[162:165]
	v_lshl_or_b32 v122, v130, 10, v198
	ds_read_b128 v[122:125], v122
	v_lshl_or_b32 v130, v130, 8, v204
	ds_read_b128 v[130:133], v130
	ds_read_b128 v[134:137], v222
	s_waitcnt lgkmcnt(0)
	v_mfma_f32_16x16x32_bf16 v[114:117], v[130:133], v[134:137], v[114:117]
	v_or_b32_e32 v130, 2, v138
	v_mfma_f32_16x16x32_bf16 v[106:109], v[122:125], v[134:137], v[106:109]
	v_lshl_or_b32 v122, v130, 10, v198
	ds_read_b128 v[122:125], v122
	v_lshl_or_b32 v130, v130, 8, v204
	ds_read_b128 v[130:133], v130
	ds_read_b128 v[134:137], v221
	s_waitcnt lgkmcnt(0)
	v_mfma_f32_16x16x32_bf16 v[114:117], v[130:133], v[134:137], v[114:117]
	v_or_b32_e32 v130, 3, v138
	v_mfma_f32_16x16x32_bf16 v[106:109], v[122:125], v[134:137], v[106:109]
	v_lshl_or_b32 v122, v130, 10, v198
	ds_read_b128 v[122:125], v122
	v_lshl_or_b32 v130, v130, 8, v204
	ds_read_b128 v[130:133], v130
	ds_read_b128 v[134:137], v219
	s_waitcnt lgkmcnt(0)
	v_mfma_f32_16x16x32_bf16 v[114:117], v[130:133], v[134:137], v[114:117]
	v_or_b32_e32 v130, 4, v138
	v_mfma_f32_16x16x32_bf16 v[106:109], v[122:125], v[134:137], v[106:109]
	v_lshl_or_b32 v122, v130, 10, v198
	ds_read_b128 v[122:125], v122
	v_lshl_or_b32 v130, v130, 8, v204
	ds_read_b128 v[130:133], v130
	ds_read_b128 v[134:137], v218
	s_waitcnt lgkmcnt(0)
	v_mfma_f32_16x16x32_bf16 v[114:117], v[130:133], v[134:137], v[114:117]
	v_or_b32_e32 v130, 5, v138
	v_mfma_f32_16x16x32_bf16 v[106:109], v[122:125], v[134:137], v[106:109]
	v_lshl_or_b32 v122, v130, 10, v198
	ds_read_b128 v[122:125], v122
	v_lshl_or_b32 v130, v130, 8, v204
	ds_read_b128 v[130:133], v130
	ds_read_b128 v[134:137], v217
	s_waitcnt lgkmcnt(0)
	v_mfma_f32_16x16x32_bf16 v[114:117], v[130:133], v[134:137], v[114:117]
	v_or_b32_e32 v130, 6, v138
	v_mfma_f32_16x16x32_bf16 v[106:109], v[122:125], v[134:137], v[106:109]
	v_lshl_or_b32 v122, v130, 10, v198
	ds_read_b128 v[122:125], v122
	v_lshl_or_b32 v130, v130, 8, v204
	ds_read_b128 v[130:133], v130
	ds_read_b128 v[134:137], v216
	s_waitcnt lgkmcnt(0)
	v_mfma_f32_16x16x32_bf16 v[114:117], v[130:133], v[134:137], v[114:117]
	v_or_b32_e32 v130, 7, v138
	v_mfma_f32_16x16x32_bf16 v[106:109], v[122:125], v[134:137], v[106:109]
	v_lshl_or_b32 v122, v130, 10, v198
	v_lshl_or_b32 v130, v130, 8, v204
	ds_read_b128 v[122:125], v122
	ds_read_b128 v[134:137], v130
	ds_read_b128 v[138:141], v213
	ds_write_b64 v212, v[2:3]
	s_waitcnt vmcnt(30)
	v_cvt_pk_bf16_f32 v2, v10, v11
	v_cvt_pk_bf16_f32 v3, v12, v13
	ds_write_b64 v211, v[2:3] offset:512
	s_waitcnt vmcnt(29)
	v_cvt_pk_bf16_f32 v2, v14, v15
	v_cvt_pk_bf16_f32 v3, v16, v17
	ds_write_b64 v210, v[2:3] offset:1024
	s_waitcnt vmcnt(28)
	v_cvt_pk_bf16_f32 v2, v22, v23
	v_cvt_pk_bf16_f32 v3, v24, v25
	ds_write_b64 v209, v[2:3] offset:1536
	s_waitcnt vmcnt(27)
	v_cvt_pk_bf16_f32 v2, v30, v31
	v_cvt_pk_bf16_f32 v3, v32, v33
	ds_write_b64 v208, v[2:3] offset:2048
	s_waitcnt vmcnt(26)
	v_cvt_pk_bf16_f32 v2, v38, v39
	v_cvt_pk_bf16_f32 v3, v40, v41
	ds_write_b64 v207, v[2:3] offset:2560
	s_waitcnt vmcnt(25)
	v_cvt_pk_bf16_f32 v2, v46, v47
	v_cvt_pk_bf16_f32 v3, v48, v49
	ds_write_b64 v206, v[2:3] offset:3072
	s_waitcnt vmcnt(24)
	v_cvt_pk_bf16_f32 v2, v54, v55
	v_cvt_pk_bf16_f32 v3, v56, v57
	ds_write_b64 v205, v[2:3] offset:3584
	s_waitcnt vmcnt(23)
	v_cvt_pk_bf16_f32 v2, v62, v63
	v_cvt_pk_bf16_f32 v3, v64, v65
	ds_write_b64 v231, v[2:3] offset:4096
	s_waitcnt vmcnt(22)
	v_cvt_pk_bf16_f32 v2, v70, v71
	v_cvt_pk_bf16_f32 v3, v72, v73
	ds_write_b64 v230, v[2:3] offset:4608
	s_waitcnt vmcnt(21)
	v_cvt_pk_bf16_f32 v2, v78, v79
	v_cvt_pk_bf16_f32 v3, v80, v81
	ds_write_b64 v229, v[2:3] offset:5120
	s_waitcnt vmcnt(20)
	v_cvt_pk_bf16_f32 v2, v86, v87
	v_cvt_pk_bf16_f32 v3, v88, v89
	ds_write_b64 v228, v[2:3] offset:5632
	s_waitcnt vmcnt(19)
	v_cvt_pk_bf16_f32 v2, v94, v95
	v_cvt_pk_bf16_f32 v3, v96, v97
	ds_write_b64 v227, v[2:3] offset:6144
	s_waitcnt vmcnt(18)
	v_cvt_pk_bf16_f32 v2, v146, v147
	v_cvt_pk_bf16_f32 v3, v148, v149
	ds_write_b64 v226, v[2:3] offset:6656
	s_waitcnt vmcnt(17)
	v_cvt_pk_bf16_f32 v2, v150, v151
	v_cvt_pk_bf16_f32 v3, v152, v153
	ds_write_b64 v225, v[2:3] offset:7168
	s_waitcnt vmcnt(16)
	v_cvt_pk_bf16_f32 v2, v154, v155
	v_cvt_pk_bf16_f32 v3, v156, v157
	ds_write_b64 v224, v[2:3] offset:7680
	v_lshlrev_b32_e32 v2, 10, v234
	s_waitcnt lgkmcnt(14)
	v_mfma_f32_16x16x32_bf16 v[130:133], v[122:125], v[138:141], v[106:109]
	v_and_or_b32 v122, v2, s0, v203
	buffer_load_dwordx4 v[2:5], v122, s[4:7], 0 offen nt
	v_or_b32_e32 v10, 0x2000, v122
	v_mfma_f32_16x16x32_bf16 v[134:137], v[134:137], v[138:141], v[114:117]
	v_or_b32_e32 v14, 0x4000, v122
	v_or_b32_e32 v22, 0x6000, v122
	v_or_b32_e32 v30, 0x8000, v122
	v_or_b32_e32 v38, 0xa000, v122
	v_or_b32_e32 v46, 0xc000, v122
	v_or_b32_e32 v54, 0xe000, v122
	v_or_b32_e32 v62, 0x10000, v122
	v_or_b32_e32 v70, 0x12000, v122
	v_or_b32_e32 v78, 0x14000, v122
	v_or_b32_e32 v86, 0x16000, v122
	v_or_b32_e32 v94, 0x18000, v122
	v_or_b32_e32 v106, 0x1a000, v122
	v_or_b32_e32 v114, 0x1c000, v122
	v_or_b32_e32 v122, 0x1e000, v122
	buffer_load_dwordx4 v[54:57], v54, s[4:7], 0 offen nt
	s_nop 0
	buffer_load_dwordx4 v[62:65], v62, s[4:7], 0 offen nt
	s_nop 0
	buffer_load_dwordx4 v[70:73], v70, s[4:7], 0 offen nt
	s_nop 0
	buffer_load_dwordx4 v[78:81], v78, s[4:7], 0 offen nt
	s_nop 0
	buffer_load_dwordx4 v[86:89], v86, s[4:7], 0 offen nt
	s_nop 0
	buffer_load_dwordx4 v[94:97], v94, s[4:7], 0 offen nt
	s_nop 0
	buffer_load_dwordx4 v[106:109], v106, s[4:7], 0 offen nt
	s_nop 0
	buffer_load_dwordx4 v[114:117], v114, s[4:7], 0 offen nt
	s_nop 0
	buffer_load_dwordx4 v[122:125], v122, s[4:7], 0 offen nt
	s_nop 0
	buffer_load_dwordx4 v[10:13], v10, s[4:7], 0 offen nt
	s_nop 0
	buffer_load_dwordx4 v[14:17], v14, s[4:7], 0 offen nt
	s_nop 0
	buffer_load_dwordx4 v[22:25], v22, s[4:7], 0 offen nt
	s_nop 0
	buffer_load_dwordx4 v[30:33], v30, s[4:7], 0 offen nt
	s_nop 0
	buffer_load_dwordx4 v[38:41], v38, s[4:7], 0 offen nt
	s_nop 0
	buffer_load_dwordx4 v[46:49], v46, s[4:7], 0 offen nt
	v_lshlrev_b32_e32 v138, 3, v235
	v_and_b32_e32 v150, 56, v138
	v_lshl_or_b32 v138, v150, 10, v198
	ds_read_b128 v[138:141], v138
	v_lshl_or_b32 v142, v150, 8, v204
	ds_read_b128 v[142:145], v142
	ds_read_b128 v[146:149], v223
	s_waitcnt vmcnt(19)
	v_cvt_pk_bf16_f32 v6, v6, v7
	v_cvt_pk_bf16_f32 v7, v8, v9
	s_waitcnt lgkmcnt(0)
	v_mfma_f32_16x16x32_bf16 v[134:137], v[142:145], v[146:149], v[134:137]
	v_or_b32_e32 v142, 1, v150
	v_mfma_f32_16x16x32_bf16 v[130:133], v[138:141], v[146:149], v[130:133]
	v_lshl_or_b32 v138, v142, 10, v198
	ds_read_b128 v[138:141], v138
	v_lshl_or_b32 v142, v142, 8, v204
	ds_read_b128 v[142:145], v142
	ds_read_b128 v[146:149], v222
	s_waitcnt lgkmcnt(0)
	v_mfma_f32_16x16x32_bf16 v[134:137], v[142:145], v[146:149], v[134:137]
	v_or_b32_e32 v142, 2, v150
	v_mfma_f32_16x16x32_bf16 v[130:133], v[138:141], v[146:149], v[130:133]
	v_lshl_or_b32 v138, v142, 10, v198
	ds_read_b128 v[138:141], v138
	v_lshl_or_b32 v142, v142, 8, v204
	ds_read_b128 v[142:145], v142
	ds_read_b128 v[146:149], v221
	s_waitcnt lgkmcnt(0)
	v_mfma_f32_16x16x32_bf16 v[134:137], v[142:145], v[146:149], v[134:137]
	v_or_b32_e32 v142, 3, v150
	v_mfma_f32_16x16x32_bf16 v[130:133], v[138:141], v[146:149], v[130:133]
	v_lshl_or_b32 v138, v142, 10, v198
	ds_read_b128 v[138:141], v138
	v_lshl_or_b32 v142, v142, 8, v204
	ds_read_b128 v[142:145], v142
	ds_read_b128 v[146:149], v219
	s_waitcnt lgkmcnt(0)
	v_mfma_f32_16x16x32_bf16 v[134:137], v[142:145], v[146:149], v[134:137]
	v_or_b32_e32 v142, 4, v150
	v_mfma_f32_16x16x32_bf16 v[130:133], v[138:141], v[146:149], v[130:133]
	v_lshl_or_b32 v138, v142, 10, v198
	ds_read_b128 v[138:141], v138
	v_lshl_or_b32 v142, v142, 8, v204
	ds_read_b128 v[142:145], v142
	ds_read_b128 v[146:149], v218
	s_waitcnt lgkmcnt(0)
	v_mfma_f32_16x16x32_bf16 v[134:137], v[142:145], v[146:149], v[134:137]
	v_or_b32_e32 v142, 5, v150
	v_mfma_f32_16x16x32_bf16 v[130:133], v[138:141], v[146:149], v[130:133]
	v_lshl_or_b32 v138, v142, 10, v198
	ds_read_b128 v[138:141], v138
	v_lshl_or_b32 v142, v142, 8, v204
	ds_read_b128 v[142:145], v142
	ds_read_b128 v[146:149], v217
	s_waitcnt lgkmcnt(0)
	v_mfma_f32_16x16x32_bf16 v[134:137], v[142:145], v[146:149], v[134:137]
	v_or_b32_e32 v142, 6, v150
	v_mfma_f32_16x16x32_bf16 v[130:133], v[138:141], v[146:149], v[130:133]
	v_lshl_or_b32 v138, v142, 10, v198
	ds_read_b128 v[138:141], v138
	v_lshl_or_b32 v142, v142, 8, v204
	ds_read_b128 v[142:145], v142
	ds_read_b128 v[146:149], v216
	s_waitcnt lgkmcnt(0)
	v_mfma_f32_16x16x32_bf16 v[134:137], v[142:145], v[146:149], v[134:137]
	v_or_b32_e32 v142, 7, v150
	v_mfma_f32_16x16x32_bf16 v[130:133], v[138:141], v[146:149], v[130:133]
	v_lshl_or_b32 v138, v142, 10, v198
	v_lshl_or_b32 v142, v142, 8, v204
	ds_read_b128 v[138:141], v138
	ds_read_b128 v[142:145], v142
	ds_read_b128 v[146:149], v213
	ds_write_b64 v212, v[6:7]
	s_waitcnt vmcnt(18)
	v_cvt_pk_bf16_f32 v6, v18, v19
	v_cvt_pk_bf16_f32 v7, v20, v21
	ds_write_b64 v211, v[6:7] offset:512
	s_waitcnt vmcnt(17)
	v_cvt_pk_bf16_f32 v6, v26, v27
	v_cvt_pk_bf16_f32 v7, v28, v29
	ds_write_b64 v210, v[6:7] offset:1024
	s_waitcnt vmcnt(16)
	v_cvt_pk_bf16_f32 v6, v34, v35
	v_cvt_pk_bf16_f32 v7, v36, v37
	ds_write_b64 v209, v[6:7] offset:1536
	v_cvt_pk_bf16_f32 v6, v42, v43
	v_cvt_pk_bf16_f32 v7, v44, v45
	ds_write_b64 v208, v[6:7] offset:2048
	v_cvt_pk_bf16_f32 v6, v50, v51
	v_cvt_pk_bf16_f32 v7, v52, v53
	ds_write_b64 v207, v[6:7] offset:2560
	v_cvt_pk_bf16_f32 v6, v58, v59
	v_cvt_pk_bf16_f32 v7, v60, v61
	ds_write_b64 v206, v[6:7] offset:3072
	v_cvt_pk_bf16_f32 v6, v66, v67
	v_cvt_pk_bf16_f32 v7, v68, v69
	ds_write_b64 v205, v[6:7] offset:3584
	v_cvt_pk_bf16_f32 v6, v74, v75
	v_cvt_pk_bf16_f32 v7, v76, v77
	ds_write_b64 v231, v[6:7] offset:4096
	v_cvt_pk_bf16_f32 v6, v82, v83
	v_cvt_pk_bf16_f32 v7, v84, v85
	ds_write_b64 v230, v[6:7] offset:4608
	v_cvt_pk_bf16_f32 v6, v90, v91
	v_cvt_pk_bf16_f32 v7, v92, v93
	ds_write_b64 v229, v[6:7] offset:5120
	v_cvt_pk_bf16_f32 v6, v98, v99
	v_cvt_pk_bf16_f32 v7, v100, v101
	ds_write_b64 v228, v[6:7] offset:5632
	v_cvt_pk_bf16_f32 v6, v102, v103
	v_cvt_pk_bf16_f32 v7, v104, v105
	ds_write_b64 v227, v[6:7] offset:6144
	v_cvt_pk_bf16_f32 v6, v110, v111
	v_cvt_pk_bf16_f32 v7, v112, v113
	ds_write_b64 v226, v[6:7] offset:6656
	v_cvt_pk_bf16_f32 v6, v118, v119
	v_cvt_pk_bf16_f32 v7, v120, v121
	ds_write_b64 v225, v[6:7] offset:7168
	v_cvt_pk_bf16_f32 v6, v126, v127
	v_cvt_pk_bf16_f32 v7, v128, v129
	ds_write_b64 v224, v[6:7] offset:7680
	v_add_u32_e32 v6, 0x1800, v196
	v_and_or_b32 v126, v6, s0, v203
	buffer_load_dwordx4 v[6:9], v126, s[4:7], 0 offen nt
	v_or_b32_e32 v18, 0x2000, v126
	v_or_b32_e32 v26, 0x4000, v126
	v_or_b32_e32 v34, 0x6000, v126
	v_or_b32_e32 v42, 0x8000, v126
	v_or_b32_e32 v50, 0xa000, v126
	v_or_b32_e32 v58, 0xc000, v126
	v_or_b32_e32 v66, 0xe000, v126
	v_or_b32_e32 v74, 0x10000, v126
	v_or_b32_e32 v82, 0x12000, v126
	v_or_b32_e32 v90, 0x14000, v126
	v_or_b32_e32 v98, 0x16000, v126
	v_or_b32_e32 v102, 0x18000, v126
	v_or_b32_e32 v110, 0x1a000, v126
	v_or_b32_e32 v118, 0x1c000, v126
	v_or_b32_e32 v126, 0x1e000, v126
	buffer_load_dwordx4 v[50:53], v50, s[4:7], 0 offen nt
	s_waitcnt lgkmcnt(14)
	v_mfma_f32_16x16x32_bf16 v[130:133], v[138:141], v[146:149], v[130:133]
	buffer_load_dwordx4 v[58:61], v58, s[4:7], 0 offen nt
	s_nop 0
	buffer_load_dwordx4 v[66:69], v66, s[4:7], 0 offen nt
	v_mfma_f32_16x16x32_bf16 v[134:137], v[142:145], v[146:149], v[134:137]
	buffer_load_dwordx4 v[74:77], v74, s[4:7], 0 offen nt
	v_add_u32_e32 v142, 7, v200
	buffer_load_dwordx4 v[82:85], v82, s[4:7], 0 offen nt
	s_nop 0
	buffer_load_dwordx4 v[90:93], v90, s[4:7], 0 offen nt
	s_nop 0
	buffer_load_dwordx4 v[98:101], v98, s[4:7], 0 offen nt
	s_nop 0
	buffer_load_dwordx4 v[102:105], v102, s[4:7], 0 offen nt
	s_nop 0
	buffer_load_dwordx4 v[110:113], v110, s[4:7], 0 offen nt
	s_nop 0
	buffer_load_dwordx4 v[118:121], v118, s[4:7], 0 offen nt
	s_nop 0
	buffer_load_dwordx4 v[126:129], v126, s[4:7], 0 offen nt
	s_nop 0
	buffer_load_dwordx4 v[18:21], v18, s[4:7], 0 offen nt
	s_nop 0
	buffer_load_dwordx4 v[26:29], v26, s[4:7], 0 offen nt
	s_nop 0
	buffer_load_dwordx4 v[34:37], v34, s[4:7], 0 offen nt
	s_nop 0
	buffer_load_dwordx4 v[42:45], v42, s[4:7], 0 offen nt
	v_xor_b32_e32 v143, 32, v232
	v_lshl_or_b32 v138, v143, 10, v198
	ds_read_b128 v[138:141], v138
	v_lshl_or_b32 v143, v143, 8, v204
	ds_read_b128 v[144:147], v143
	ds_read_b128 v[148:151], v223
	v_bitop3_b32 v143, v232, 1, 32 bitop3:0xde
	s_waitcnt vmcnt(31)
	v_cvt_pk_bf16_f32 v2, v2, v3
	s_waitcnt lgkmcnt(0)
	v_mfma_f32_16x16x32_bf16 v[134:137], v[144:147], v[148:151], v[134:137]
	v_cvt_pk_bf16_f32 v3, v4, v5
	v_mfma_f32_16x16x32_bf16 v[130:133], v[138:141], v[148:151], v[130:133]
	v_lshl_or_b32 v138, v143, 10, v198
	ds_read_b128 v[138:141], v138
	v_lshl_or_b32 v143, v143, 8, v204
	ds_read_b128 v[144:147], v143
	ds_read_b128 v[148:151], v222
	v_bitop3_b32 v143, v232, 2, 32 bitop3:0xde
	s_waitcnt lgkmcnt(0)
	v_mfma_f32_16x16x32_bf16 v[134:137], v[144:147], v[148:151], v[134:137]
	v_mfma_f32_16x16x32_bf16 v[130:133], v[138:141], v[148:151], v[130:133]
	v_lshl_or_b32 v138, v143, 10, v198
	ds_read_b128 v[138:141], v138
	v_lshl_or_b32 v143, v143, 8, v204
	ds_read_b128 v[144:147], v143
	ds_read_b128 v[148:151], v221
	v_bitop3_b32 v143, v232, 3, 32 bitop3:0xde
	s_waitcnt lgkmcnt(0)
	v_mfma_f32_16x16x32_bf16 v[130:133], v[138:141], v[148:151], v[130:133]
	v_lshl_or_b32 v138, v143, 10, v198
	ds_read_b128 v[138:141], v138
	v_lshl_or_b32 v143, v143, 8, v204
	v_mfma_f32_16x16x32_bf16 v[134:137], v[144:147], v[148:151], v[134:137]
	ds_read_b128 v[144:147], v143
	ds_read_b128 v[148:151], v219
	v_bitop3_b32 v143, v232, 4, 32 bitop3:0xde
	s_waitcnt lgkmcnt(0)
	v_mfma_f32_16x16x32_bf16 v[130:133], v[138:141], v[148:151], v[130:133]
	v_lshl_or_b32 v138, v143, 10, v198
	ds_read_b128 v[138:141], v138
	v_lshl_or_b32 v143, v143, 8, v204
	v_mfma_f32_16x16x32_bf16 v[134:137], v[144:147], v[148:151], v[134:137]
	ds_read_b128 v[144:147], v143
	ds_read_b128 v[148:151], v218
	v_bitop3_b32 v143, v232, 5, 32 bitop3:0xde
	s_waitcnt lgkmcnt(0)
	v_mfma_f32_16x16x32_bf16 v[130:133], v[138:141], v[148:151], v[130:133]
	v_lshl_or_b32 v138, v143, 10, v198
	ds_read_b128 v[138:141], v138
	v_lshl_or_b32 v143, v143, 8, v204
	v_mfma_f32_16x16x32_bf16 v[134:137], v[144:147], v[148:151], v[134:137]
	ds_read_b128 v[144:147], v143
	ds_read_b128 v[148:151], v217
	v_bitop3_b32 v143, v232, 6, 32 bitop3:0xde
	s_waitcnt lgkmcnt(0)
	v_mfma_f32_16x16x32_bf16 v[130:133], v[138:141], v[148:151], v[130:133]
	v_lshl_or_b32 v138, v143, 10, v198
	ds_read_b128 v[138:141], v138
	v_lshl_or_b32 v143, v143, 8, v204
	v_mfma_f32_16x16x32_bf16 v[134:137], v[144:147], v[148:151], v[134:137]
	ds_read_b128 v[144:147], v143
	ds_read_b128 v[148:151], v216
	v_bitop3_b32 v143, v232, 7, 32 bitop3:0xde
	s_waitcnt lgkmcnt(0)
	v_mfma_f32_16x16x32_bf16 v[130:133], v[138:141], v[148:151], v[130:133]
	v_lshl_or_b32 v138, v143, 10, v198
	v_lshl_or_b32 v143, v143, 8, v204
	ds_read_b128 v[138:141], v138
	v_mfma_f32_16x16x32_bf16 v[134:137], v[144:147], v[148:151], v[134:137]
	ds_read_b128 v[144:147], v143
	ds_read_b128 v[148:151], v213
	ds_write_b64 v212, v[2:3]
	s_waitcnt vmcnt(21)
	v_cvt_pk_bf16_f32 v2, v10, v11
	v_cvt_pk_bf16_f32 v3, v12, v13
	ds_write_b64 v211, v[2:3] offset:512
	s_waitcnt vmcnt(20)
	v_cvt_pk_bf16_f32 v2, v14, v15
	v_cvt_pk_bf16_f32 v3, v16, v17
	ds_write_b64 v210, v[2:3] offset:1024
	s_waitcnt vmcnt(19)
	v_cvt_pk_bf16_f32 v2, v22, v23
	v_cvt_pk_bf16_f32 v3, v24, v25
	ds_write_b64 v209, v[2:3] offset:1536
	s_waitcnt vmcnt(18)
	v_cvt_pk_bf16_f32 v2, v30, v31
	v_cvt_pk_bf16_f32 v3, v32, v33
	ds_write_b64 v208, v[2:3] offset:2048
	s_waitcnt vmcnt(17)
	v_cvt_pk_bf16_f32 v2, v38, v39
	v_cvt_pk_bf16_f32 v3, v40, v41
	ds_write_b64 v207, v[2:3] offset:2560
	s_waitcnt vmcnt(16)
	v_cvt_pk_bf16_f32 v2, v46, v47
	v_cvt_pk_bf16_f32 v3, v48, v49
	ds_write_b64 v206, v[2:3] offset:3072
	v_cvt_pk_bf16_f32 v2, v54, v55
	v_cvt_pk_bf16_f32 v3, v56, v57
	ds_write_b64 v205, v[2:3] offset:3584
	v_cvt_pk_bf16_f32 v2, v62, v63
	v_cvt_pk_bf16_f32 v3, v64, v65
	ds_write_b64 v231, v[2:3] offset:4096
	v_cvt_pk_bf16_f32 v2, v70, v71
	v_cvt_pk_bf16_f32 v3, v72, v73
	ds_write_b64 v230, v[2:3] offset:4608
	v_cvt_pk_bf16_f32 v2, v78, v79
	v_cvt_pk_bf16_f32 v3, v80, v81
	ds_write_b64 v229, v[2:3] offset:5120
	v_cvt_pk_bf16_f32 v2, v86, v87
	v_cvt_pk_bf16_f32 v3, v88, v89
	ds_write_b64 v228, v[2:3] offset:5632
	v_cvt_pk_bf16_f32 v2, v94, v95
	v_cvt_pk_bf16_f32 v3, v96, v97
	ds_write_b64 v227, v[2:3] offset:6144
	v_cvt_pk_bf16_f32 v2, v106, v107
	v_cvt_pk_bf16_f32 v3, v108, v109
	ds_write_b64 v226, v[2:3] offset:6656
	v_cvt_pk_bf16_f32 v2, v114, v115
	v_cvt_pk_bf16_f32 v3, v116, v117
	ds_write_b64 v225, v[2:3] offset:7168
	v_cvt_pk_bf16_f32 v2, v122, v123
	v_cvt_pk_bf16_f32 v3, v124, v125
	ds_write_b64 v224, v[2:3] offset:7680
	v_lshlrev_b32_e32 v2, 10, v142
	v_and_or_b32 v2, v2, s0, v203
	v_or_b32_e32 v3, 0x2000, v2
	buffer_load_dwordx4 v[10:13], v2, s[4:7], 0 offen nt
	buffer_load_dwordx4 v[14:17], v3, s[4:7], 0 offen nt
	v_or_b32_e32 v3, 0x4000, v2
	buffer_load_dwordx4 v[22:25], v3, s[4:7], 0 offen nt
	v_or_b32_e32 v3, 0x6000, v2
	buffer_load_dwordx4 v[30:33], v3, s[4:7], 0 offen nt
	v_or_b32_e32 v3, 0x8000, v2
	buffer_load_dwordx4 v[38:41], v3, s[4:7], 0 offen nt
	v_or_b32_e32 v3, 0xa000, v2
	buffer_load_dwordx4 v[46:49], v3, s[4:7], 0 offen nt
	v_or_b32_e32 v3, 0xc000, v2
	buffer_load_dwordx4 v[54:57], v3, s[4:7], 0 offen nt
	v_or_b32_e32 v3, 0xe000, v2
	buffer_load_dwordx4 v[62:65], v3, s[4:7], 0 offen nt
	v_or_b32_e32 v3, 0x10000, v2
	buffer_load_dwordx4 v[70:73], v3, s[4:7], 0 offen nt
	v_or_b32_e32 v3, 0x12000, v2
	buffer_load_dwordx4 v[78:81], v3, s[4:7], 0 offen nt
	v_or_b32_e32 v3, 0x14000, v2
	buffer_load_dwordx4 v[86:89], v3, s[4:7], 0 offen nt
	v_or_b32_e32 v3, 0x16000, v2
	buffer_load_dwordx4 v[94:97], v3, s[4:7], 0 offen nt
	v_or_b32_e32 v3, 0x18000, v2
	buffer_load_dwordx4 v[106:109], v3, s[4:7], 0 offen nt
	v_or_b32_e32 v3, 0x1a000, v2
	buffer_load_dwordx4 v[114:117], v3, s[4:7], 0 offen nt
	v_or_b32_e32 v3, 0x1c000, v2
	v_or_b32_e32 v2, 0x1e000, v2
	s_waitcnt lgkmcnt(14)
	v_mfma_f32_16x16x32_bf16 v[138:141], v[138:141], v[148:151], v[130:133]
	buffer_load_dwordx4 v[122:125], v3, s[4:7], 0 offen nt
	s_nop 1
	buffer_load_dwordx4 v[130:133], v2, s[4:7], 0 offen nt
	v_mfma_f32_16x16x32_bf16 v[134:137], v[144:147], v[148:151], v[134:137]
	v_lshlrev_b32_e32 v2, 3, v234
	v_and_b32_e32 v143, 56, v2
	v_lshl_or_b32 v2, v143, 10, v198
	v_lshl_or_b32 v152, v143, 8, v204
	ds_read_b128 v[2:5], v2
	ds_read_b128 v[144:147], v223
	ds_read_b128 v[148:151], v222
	ds_read_b128 v[152:155], v152
	v_or_b32_e32 v156, 1, v143
	v_lshl_or_b32 v157, v156, 10, v198
	s_waitcnt lgkmcnt(2)
	v_mfma_f32_16x16x32_bf16 v[2:5], v[2:5], v[144:147], v[138:141]
	s_waitcnt vmcnt(31)
	v_cvt_pk_bf16_f32 v6, v6, v7
	v_cvt_pk_bf16_f32 v7, v8, v9
	s_waitcnt lgkmcnt(0)
	v_mfma_f32_16x16x32_bf16 v[134:137], v[152:155], v[144:147], v[134:137]
	ds_read_b128 v[138:141], v157
	v_lshl_or_b32 v144, v156, 8, v204
	ds_read_b128 v[144:147], v144
	v_or_b32_e32 v156, 2, v143
	s_waitcnt lgkmcnt(1)
	v_mfma_f32_16x16x32_bf16 v[2:5], v[138:141], v[148:151], v[2:5]
	v_lshl_or_b32 v138, v156, 10, v198
	ds_read_b128 v[138:141], v138
	ds_read_b128 v[152:155], v221
	s_waitcnt lgkmcnt(2)
	v_mfma_f32_16x16x32_bf16 v[134:137], v[144:147], v[148:151], v[134:137]
	v_lshl_or_b32 v144, v156, 8, v204
	v_or_b32_e32 v156, 3, v143
	ds_read_b128 v[144:147], v144
	ds_read_b128 v[148:151], v219
	s_waitcnt lgkmcnt(2)
	v_mfma_f32_16x16x32_bf16 v[2:5], v[138:141], v[152:155], v[2:5]
	v_lshl_or_b32 v138, v156, 10, v198
	ds_read_b128 v[138:141], v138
	s_waitcnt lgkmcnt(2)
	v_mfma_f32_16x16x32_bf16 v[134:137], v[144:147], v[152:155], v[134:137]
	v_lshl_or_b32 v144, v156, 8, v204
	ds_read_b128 v[144:147], v144
	v_or_b32_e32 v152, 4, v143
	s_waitcnt lgkmcnt(1)
	v_mfma_f32_16x16x32_bf16 v[2:5], v[138:141], v[148:151], v[2:5]
	v_lshl_or_b32 v138, v152, 10, v198
	ds_read_b128 v[138:141], v138
	v_or_b32_e32 v156, 5, v143
	s_waitcnt lgkmcnt(1)
	v_mfma_f32_16x16x32_bf16 v[134:137], v[144:147], v[148:151], v[134:137]
	ds_read_b128 v[144:147], v218
	v_lshl_or_b32 v148, v152, 8, v204
	ds_read_b128 v[148:151], v148
	ds_read_b128 v[152:155], v217
	s_waitcnt lgkmcnt(2)
	v_mfma_f32_16x16x32_bf16 v[2:5], v[138:141], v[144:147], v[2:5]
	v_lshl_or_b32 v138, v156, 10, v198
	ds_read_b128 v[138:141], v138
	s_waitcnt lgkmcnt(2)
	v_mfma_f32_16x16x32_bf16 v[134:137], v[148:151], v[144:147], v[134:137]
	v_lshl_or_b32 v144, v156, 8, v204
	ds_read_b128 v[144:147], v144
	v_or_b32_e32 v148, 6, v143
	s_waitcnt lgkmcnt(1)
	v_mfma_f32_16x16x32_bf16 v[2:5], v[138:141], v[152:155], v[2:5]
	v_lshl_or_b32 v138, v148, 10, v198
	ds_read_b128 v[138:141], v138
	v_lshl_or_b32 v148, v148, 8, v204
	s_waitcnt lgkmcnt(1)
	v_mfma_f32_16x16x32_bf16 v[134:137], v[144:147], v[152:155], v[134:137]
	ds_read_b128 v[144:147], v216
	ds_read_b128 v[148:151], v148
	ds_read_b128 v[152:155], v213
	v_or_b32_e32 v143, 7, v143
	ds_write_b64 v212, v[6:7]
	s_waitcnt lgkmcnt(3)
	v_mfma_f32_16x16x32_bf16 v[2:5], v[138:141], v[144:147], v[2:5]
	v_lshl_or_b32 v138, v143, 10, v198
	v_lshl_or_b32 v143, v143, 8, v204
	s_waitcnt vmcnt(19)
	v_cvt_pk_bf16_f32 v6, v18, v19
	v_cvt_pk_bf16_f32 v7, v20, v21
	ds_read_b128 v[138:141], v138
	s_waitcnt lgkmcnt(3)
	v_mfma_f32_16x16x32_bf16 v[134:137], v[148:151], v[144:147], v[134:137]
	ds_read_b128 v[144:147], v143
	ds_write_b64 v211, v[6:7] offset:512
	s_waitcnt vmcnt(18)
	v_cvt_pk_bf16_f32 v6, v26, v27
	v_cvt_pk_bf16_f32 v7, v28, v29
	ds_write_b64 v210, v[6:7] offset:1024
	s_waitcnt vmcnt(17)
	v_cvt_pk_bf16_f32 v6, v34, v35
	v_cvt_pk_bf16_f32 v7, v36, v37
	ds_write_b64 v209, v[6:7] offset:1536
	s_waitcnt vmcnt(16)
	v_cvt_pk_bf16_f32 v6, v42, v43
	v_cvt_pk_bf16_f32 v7, v44, v45
	ds_write_b64 v208, v[6:7] offset:2048
	v_cvt_pk_bf16_f32 v6, v50, v51
	v_cvt_pk_bf16_f32 v7, v52, v53
	ds_write_b64 v207, v[6:7] offset:2560
	v_cvt_pk_bf16_f32 v6, v58, v59
	v_cvt_pk_bf16_f32 v7, v60, v61
	ds_write_b64 v206, v[6:7] offset:3072
	v_cvt_pk_bf16_f32 v6, v66, v67
	v_cvt_pk_bf16_f32 v7, v68, v69
	ds_write_b64 v205, v[6:7] offset:3584
	v_cvt_pk_bf16_f32 v6, v74, v75
	v_cvt_pk_bf16_f32 v7, v76, v77
	ds_write_b64 v231, v[6:7] offset:4096
	v_cvt_pk_bf16_f32 v6, v82, v83
	v_cvt_pk_bf16_f32 v7, v84, v85
	ds_write_b64 v230, v[6:7] offset:4608
	v_cvt_pk_bf16_f32 v6, v90, v91
	v_cvt_pk_bf16_f32 v7, v92, v93
	s_waitcnt lgkmcnt(9)
	v_mfma_f32_16x16x32_bf16 v[134:137], v[144:147], v[152:155], v[134:137]
	ds_write_b64 v229, v[6:7] offset:5120
	v_cvt_pk_bf16_f32 v6, v98, v99
	v_cvt_pk_bf16_f32 v7, v100, v101
	ds_write_b64 v228, v[6:7] offset:5632
	v_cvt_pk_bf16_f32 v6, v102, v103
	v_cvt_pk_bf16_f32 v7, v104, v105
	ds_write_b64 v227, v[6:7] offset:6144
	v_cvt_pk_bf16_f32 v6, v110, v111
	v_cvt_pk_bf16_f32 v7, v112, v113
	ds_write_b64 v226, v[6:7] offset:6656
	v_cvt_pk_bf16_f32 v6, v118, v119
	v_cvt_pk_bf16_f32 v7, v120, v121
	v_mfma_f32_16x16x32_bf16 v[2:5], v[138:141], v[152:155], v[2:5]
	ds_write_b64 v225, v[6:7] offset:7168
	v_cvt_pk_bf16_f32 v6, v126, v127
	v_cvt_pk_bf16_f32 v7, v128, v129
	ds_write_b64 v224, v[6:7] offset:7680
	v_add_u32_e32 v6, 48, v232
	v_and_b32_e32 v50, 56, v6
	v_lshl_or_b32 v6, v50, 10, v198
	v_lshl_or_b32 v34, v50, 8, v204
	ds_read_b128 v[6:9], v6
	ds_read_b128 v[18:21], v223
	ds_read_b128 v[26:29], v222
	ds_read_b128 v[34:37], v34
	v_or_b32_e32 v42, 1, v50
	v_lshl_or_b32 v43, v42, 10, v198
	s_waitcnt lgkmcnt(2)
	v_mfma_f32_16x16x32_bf16 v[2:5], v[6:9], v[18:21], v[2:5]
	ds_read_b128 v[6:9], v43
	v_or_b32_e32 v51, 2, v50
	s_waitcnt lgkmcnt(1)
	v_mfma_f32_16x16x32_bf16 v[18:21], v[34:37], v[18:21], v[134:137]
	v_lshl_or_b32 v34, v42, 8, v204
	ds_read_b128 v[34:37], v34
	s_waitcnt lgkmcnt(1)
	v_mfma_f32_16x16x32_bf16 v[2:5], v[6:9], v[26:29], v[2:5]
	v_lshl_or_b32 v6, v51, 10, v198
	ds_read_b128 v[6:9], v6
	ds_read_b128 v[42:45], v221
	s_waitcnt lgkmcnt(2)
	v_mfma_f32_16x16x32_bf16 v[18:21], v[34:37], v[26:29], v[18:21]
	v_lshl_or_b32 v26, v51, 8, v204
	v_or_b32_e32 v51, 3, v50
	ds_read_b128 v[26:29], v26
	ds_read_b128 v[34:37], v219
	s_waitcnt lgkmcnt(2)
	v_mfma_f32_16x16x32_bf16 v[2:5], v[6:9], v[42:45], v[2:5]
	v_lshl_or_b32 v6, v51, 10, v198
	ds_read_b128 v[6:9], v6
	s_waitcnt lgkmcnt(2)
	v_mfma_f32_16x16x32_bf16 v[18:21], v[26:29], v[42:45], v[18:21]
	v_lshl_or_b32 v26, v51, 8, v204
	ds_read_b128 v[26:29], v26
	v_or_b32_e32 v42, 4, v50
	s_waitcnt lgkmcnt(1)
	v_mfma_f32_16x16x32_bf16 v[2:5], v[6:9], v[34:37], v[2:5]
	v_lshl_or_b32 v6, v42, 10, v198
	ds_read_b128 v[6:9], v6
	v_or_b32_e32 v51, 5, v50
	s_waitcnt lgkmcnt(1)
	v_mfma_f32_16x16x32_bf16 v[18:21], v[26:29], v[34:37], v[18:21]
	ds_read_b128 v[26:29], v218
	v_lshl_or_b32 v34, v42, 8, v204
	ds_read_b128 v[34:37], v34
	ds_read_b128 v[42:45], v217
	s_waitcnt lgkmcnt(2)
	v_mfma_f32_16x16x32_bf16 v[2:5], v[6:9], v[26:29], v[2:5]
	v_lshl_or_b32 v6, v51, 10, v198
	ds_read_b128 v[6:9], v6
	s_waitcnt lgkmcnt(2)
	v_mfma_f32_16x16x32_bf16 v[18:21], v[34:37], v[26:29], v[18:21]
	v_lshl_or_b32 v26, v51, 8, v204
	ds_read_b128 v[26:29], v26
	v_or_b32_e32 v34, 6, v50
	s_waitcnt lgkmcnt(1)
	v_mfma_f32_16x16x32_bf16 v[2:5], v[6:9], v[42:45], v[2:5]
	v_lshl_or_b32 v6, v34, 10, v198
	ds_read_b128 v[6:9], v6
	v_lshl_or_b32 v34, v34, 8, v204
	s_waitcnt lgkmcnt(1)
	v_mfma_f32_16x16x32_bf16 v[18:21], v[26:29], v[42:45], v[18:21]
	ds_read_b128 v[26:29], v216
	ds_read_b128 v[34:37], v34
	ds_read_b128 v[42:45], v213
	v_or_b32_e32 v50, 7, v50
	s_waitcnt lgkmcnt(2)
	v_mfma_f32_16x16x32_bf16 v[2:5], v[6:9], v[26:29], v[2:5]
	v_lshl_or_b32 v6, v50, 10, v198
	ds_read_b128 v[6:9], v6
	s_waitcnt lgkmcnt(2)
	v_mfma_f32_16x16x32_bf16 v[18:21], v[34:37], v[26:29], v[18:21]
	v_lshl_or_b32 v26, v50, 8, v204
	ds_read_b128 v[26:29], v26
	s_waitcnt lgkmcnt(1)
	v_mfma_f32_16x16x32_bf16 v[34:37], v[6:9], v[42:45], v[2:5]
	v_and_b32_e32 v74, 7, v197
	v_lshrrev_b32_e32 v75, 3, v197
	v_lshlrev_b32_e32 v192, 13, v200
	v_lshlrev_b32_e32 v193, 11, v200
	v_lshl_add_u32 v203, v197, 2, v196
	v_lshl_or_b32 v192, v75, 8, v192
	v_lshl_or_b32 v193, v75, 6, v193
	v_add_u32_e32 v203, 0x24800, v203
	v_lshl_or_b32 v192, v201, 6, v192
	v_lshl_or_b32 v193, v74, 1, v193
	v_lshl_or_b32 v192, v74, 1, v192
	v_or_b32_e32 v193, 0x10000, v193
	v_cmp_gt_u32_e64 s[36:37], 16, v1
	v_cmp_eq_u32_e64 s[38:39], 1, v201
	ds_read2_b32 v[2:3], v203 offset1:16
	ds_read2_b32 v[4:5], v203 offset0:32 offset1:48
	ds_read2_b32 v[6:7], v203 offset0:64 offset1:80
	ds_read2_b32 v[8:9], v203 offset0:96 offset1:112
	ds_read2_b32 v[50:51], v203 offset0:128 offset1:144
	ds_read2_b32 v[52:53], v203 offset0:160 offset1:176
	ds_read2_b32 v[58:59], v203 offset0:192 offset1:208
	ds_read2_b32 v[60:61], v203 offset0:224 offset1:240
	v_mov_b32_e32 v146, 0
	v_mov_b32_e32 v147, 0
	v_mov_b32_e32 v150, 0
	v_mov_b32_e32 v151, 0
	v_mov_b32_e32 v154, 0
	v_mov_b32_e32 v155, 0
	v_mov_b32_e32 v158, 0
	v_mov_b32_e32 v159, 0
	v_mov_b32_e32 v162, 0
	v_mov_b32_e32 v163, 0
	v_mov_b32_e32 v166, 0
	v_mov_b32_e32 v167, 0
	v_mov_b32_e32 v170, 0
	v_mov_b32_e32 v171, 0
	v_mov_b32_e32 v174, 0
	v_mov_b32_e32 v175, 0
	v_mov_b32_e32 v178, 0
	v_mov_b32_e32 v179, 0
	v_mov_b32_e32 v182, 0
	v_mov_b32_e32 v183, 0
	v_mov_b32_e32 v186, 0
	v_mov_b32_e32 v187, 0
	v_mov_b32_e32 v190, 0
	v_mov_b32_e32 v191, 0
	v_mov_b32_e32 v234, 0
	v_mov_b32_e32 v235, 0
	v_mov_b32_e32 v238, 0
	v_mov_b32_e32 v239, 0
	v_mov_b32_e32 v242, 0
	v_mov_b32_e32 v243, 0
	v_mov_b32_e32 v246, 0
	v_mov_b32_e32 v247, 0
	ds_read_u16 v82, v192
	ds_read_u16 v83, v192 offset:16
	ds_read_u16 v84, v192 offset:32
	ds_read_u16 v85, v192 offset:48
	ds_read_u16 v90, v193
	ds_read_u16 v91, v193 offset:16
	ds_read_u16 v92, v193 offset:32
	ds_read_u16 v93, v193 offset:48
	ds_read_u16 v98, v192 offset:512
	ds_read_u16 v99, v192 offset:528
	ds_read_u16 v100, v192 offset:544
	ds_read_u16 v101, v192 offset:560
	ds_read_u16 v102, v193 offset:128
	ds_read_u16 v103, v193 offset:144
	ds_read_u16 v104, v193 offset:160
	ds_read_u16 v105, v193 offset:176
	s_waitcnt lgkmcnt(8)
	v_lshl_or_b32 v144, v83, 16, v82
	v_lshl_or_b32 v145, v85, 16, v84
	s_mov_b64 exec, s[36:37]
	v_lshl_or_b32 v146, v91, 16, v90
	v_lshl_or_b32 v147, v93, 16, v92
	s_mov_b64 exec, -1
	ds_read_u16 v82, v192 offset:1024
	ds_read_u16 v83, v192 offset:1040
	ds_read_u16 v84, v192 offset:1056
	ds_read_u16 v85, v192 offset:1072
	ds_read_u16 v90, v193 offset:256
	ds_read_u16 v91, v193 offset:272
	ds_read_u16 v92, v193 offset:288
	ds_read_u16 v93, v193 offset:304
	s_waitcnt lgkmcnt(8)
	v_lshl_or_b32 v148, v99, 16, v98
	v_lshl_or_b32 v149, v101, 16, v100
	s_mov_b64 exec, s[36:37]
	v_lshl_or_b32 v150, v103, 16, v102
	v_lshl_or_b32 v151, v105, 16, v104
	s_mov_b64 exec, -1
	ds_read_u16 v98, v192 offset:1536
	ds_read_u16 v99, v192 offset:1552
	ds_read_u16 v100, v192 offset:1568
	ds_read_u16 v101, v192 offset:1584
	ds_read_u16 v102, v193 offset:384
	ds_read_u16 v103, v193 offset:400
	ds_read_u16 v104, v193 offset:416
	ds_read_u16 v105, v193 offset:432
	s_waitcnt lgkmcnt(8)
	v_lshl_or_b32 v152, v83, 16, v82
	v_lshl_or_b32 v153, v85, 16, v84
	s_mov_b64 exec, s[36:37]
	v_lshl_or_b32 v154, v91, 16, v90
	v_lshl_or_b32 v155, v93, 16, v92
	s_mov_b64 exec, -1
	ds_read_u16 v82, v192 offset:2048
	ds_read_u16 v83, v192 offset:2064
	ds_read_u16 v84, v192 offset:2080
	ds_read_u16 v85, v192 offset:2096
	ds_read_u16 v90, v193 offset:512
	ds_read_u16 v91, v193 offset:528
	ds_read_u16 v92, v193 offset:544
	ds_read_u16 v93, v193 offset:560
	s_waitcnt lgkmcnt(8)
	v_lshl_or_b32 v156, v99, 16, v98
	v_lshl_or_b32 v157, v101, 16, v100
	s_mov_b64 exec, s[36:37]
	v_lshl_or_b32 v158, v103, 16, v102
	v_lshl_or_b32 v159, v105, 16, v104
	s_mov_b64 exec, -1
	ds_read_u16 v98, v192 offset:2560
	ds_read_u16 v99, v192 offset:2576
	ds_read_u16 v100, v192 offset:2592
	ds_read_u16 v101, v192 offset:2608
	ds_read_u16 v102, v193 offset:640
	ds_read_u16 v103, v193 offset:656
	ds_read_u16 v104, v193 offset:672
	ds_read_u16 v105, v193 offset:688
	s_waitcnt lgkmcnt(8)
	v_lshl_or_b32 v160, v83, 16, v82
	v_lshl_or_b32 v161, v85, 16, v84
	s_mov_b64 exec, s[36:37]
	v_lshl_or_b32 v162, v91, 16, v90
	v_lshl_or_b32 v163, v93, 16, v92
	s_mov_b64 exec, -1
	ds_read_u16 v82, v192 offset:3072
	ds_read_u16 v83, v192 offset:3088
	ds_read_u16 v84, v192 offset:3104
	ds_read_u16 v85, v192 offset:3120
	ds_read_u16 v90, v193 offset:768
	ds_read_u16 v91, v193 offset:784
	ds_read_u16 v92, v193 offset:800
	ds_read_u16 v93, v193 offset:816
	s_waitcnt lgkmcnt(8)
	v_lshl_or_b32 v164, v99, 16, v98
	v_lshl_or_b32 v165, v101, 16, v100
	s_mov_b64 exec, s[36:37]
	v_lshl_or_b32 v166, v103, 16, v102
	v_lshl_or_b32 v167, v105, 16, v104
	s_mov_b64 exec, -1
	ds_read_u16 v98, v192 offset:3584
	ds_read_u16 v99, v192 offset:3600
	ds_read_u16 v100, v192 offset:3616
	ds_read_u16 v101, v192 offset:3632
	ds_read_u16 v102, v193 offset:896
	ds_read_u16 v103, v193 offset:912
	ds_read_u16 v104, v193 offset:928
	ds_read_u16 v105, v193 offset:944
	s_waitcnt lgkmcnt(8)
	v_lshl_or_b32 v168, v83, 16, v82
	v_lshl_or_b32 v169, v85, 16, v84
	s_mov_b64 exec, s[36:37]
	v_lshl_or_b32 v170, v91, 16, v90
	v_lshl_or_b32 v171, v93, 16, v92
	s_mov_b64 exec, -1
	ds_read_u16 v82, v192 offset:4096
	ds_read_u16 v83, v192 offset:4112
	ds_read_u16 v84, v192 offset:4128
	ds_read_u16 v85, v192 offset:4144
	ds_read_u16 v90, v193 offset:1024
	ds_read_u16 v91, v193 offset:1040
	ds_read_u16 v92, v193 offset:1056
	ds_read_u16 v93, v193 offset:1072
	s_waitcnt lgkmcnt(8)
	v_lshl_or_b32 v172, v99, 16, v98
	v_lshl_or_b32 v173, v101, 16, v100
	s_mov_b64 exec, s[36:37]
	v_lshl_or_b32 v174, v103, 16, v102
	v_lshl_or_b32 v175, v105, 16, v104
	s_mov_b64 exec, -1
	ds_read_u16 v98, v192 offset:4608
	ds_read_u16 v99, v192 offset:4624
	ds_read_u16 v100, v192 offset:4640
	ds_read_u16 v101, v192 offset:4656
	ds_read_u16 v102, v193 offset:1152
	ds_read_u16 v103, v193 offset:1168
	ds_read_u16 v104, v193 offset:1184
	ds_read_u16 v105, v193 offset:1200
	s_waitcnt lgkmcnt(8)
	v_lshl_or_b32 v176, v83, 16, v82
	v_lshl_or_b32 v177, v85, 16, v84
	s_mov_b64 exec, s[36:37]
	v_lshl_or_b32 v178, v91, 16, v90
	v_lshl_or_b32 v179, v93, 16, v92
	s_mov_b64 exec, -1
	ds_read_u16 v82, v192 offset:5120
	ds_read_u16 v83, v192 offset:5136
	ds_read_u16 v84, v192 offset:5152
	ds_read_u16 v85, v192 offset:5168
	ds_read_u16 v90, v193 offset:1280
	ds_read_u16 v91, v193 offset:1296
	ds_read_u16 v92, v193 offset:1312
	ds_read_u16 v93, v193 offset:1328
	s_waitcnt lgkmcnt(8)
	v_lshl_or_b32 v180, v99, 16, v98
	v_lshl_or_b32 v181, v101, 16, v100
	s_mov_b64 exec, s[36:37]
	v_lshl_or_b32 v182, v103, 16, v102
	v_lshl_or_b32 v183, v105, 16, v104
	s_mov_b64 exec, -1
	ds_read_u16 v98, v192 offset:5632
	ds_read_u16 v99, v192 offset:5648
	ds_read_u16 v100, v192 offset:5664
	ds_read_u16 v101, v192 offset:5680
	ds_read_u16 v102, v193 offset:1408
	ds_read_u16 v103, v193 offset:1424
	ds_read_u16 v104, v193 offset:1440
	ds_read_u16 v105, v193 offset:1456
	s_waitcnt lgkmcnt(8)
	v_lshl_or_b32 v184, v83, 16, v82
	v_lshl_or_b32 v185, v85, 16, v84
	s_mov_b64 exec, s[36:37]
	v_lshl_or_b32 v186, v91, 16, v90
	v_lshl_or_b32 v187, v93, 16, v92
	s_mov_b64 exec, -1
	ds_read_u16 v82, v192 offset:6144
	ds_read_u16 v83, v192 offset:6160
	ds_read_u16 v84, v192 offset:6176
	ds_read_u16 v85, v192 offset:6192
	ds_read_u16 v90, v193 offset:1536
	ds_read_u16 v91, v193 offset:1552
	ds_read_u16 v92, v193 offset:1568
	ds_read_u16 v93, v193 offset:1584
	s_waitcnt lgkmcnt(8)
	v_lshl_or_b32 v188, v99, 16, v98
	v_lshl_or_b32 v189, v101, 16, v100
	s_mov_b64 exec, s[36:37]
	v_lshl_or_b32 v190, v103, 16, v102
	v_lshl_or_b32 v191, v105, 16, v104
	s_mov_b64 exec, -1
	ds_read_u16 v98, v192 offset:6656
	ds_read_u16 v99, v192 offset:6672
	ds_read_u16 v100, v192 offset:6688
	ds_read_u16 v101, v192 offset:6704
	ds_read_u16 v102, v193 offset:1664
	ds_read_u16 v103, v193 offset:1680
	ds_read_u16 v104, v193 offset:1696
	ds_read_u16 v105, v193 offset:1712
	s_waitcnt lgkmcnt(8)
	v_lshl_or_b32 v232, v83, 16, v82
	v_lshl_or_b32 v233, v85, 16, v84
	s_mov_b64 exec, s[36:37]
	v_lshl_or_b32 v234, v91, 16, v90
	v_lshl_or_b32 v235, v93, 16, v92
	s_mov_b64 exec, -1
	ds_read_u16 v82, v192 offset:7168
	ds_read_u16 v83, v192 offset:7184
	ds_read_u16 v84, v192 offset:7200
	ds_read_u16 v85, v192 offset:7216
	ds_read_u16 v90, v193 offset:1792
	ds_read_u16 v91, v193 offset:1808
	ds_read_u16 v92, v193 offset:1824
	ds_read_u16 v93, v193 offset:1840
	s_waitcnt lgkmcnt(8)
	v_lshl_or_b32 v236, v99, 16, v98
	v_lshl_or_b32 v237, v101, 16, v100
	s_mov_b64 exec, s[36:37]
	v_lshl_or_b32 v238, v103, 16, v102
	v_lshl_or_b32 v239, v105, 16, v104
	s_mov_b64 exec, -1
	ds_read_u16 v98, v192 offset:7680
	ds_read_u16 v99, v192 offset:7696
	ds_read_u16 v100, v192 offset:7712
	ds_read_u16 v101, v192 offset:7728
	ds_read_u16 v102, v193 offset:1920
	ds_read_u16 v103, v193 offset:1936
	ds_read_u16 v104, v193 offset:1952
	ds_read_u16 v105, v193 offset:1968
	s_waitcnt lgkmcnt(8)
	v_lshl_or_b32 v240, v83, 16, v82
	v_lshl_or_b32 v241, v85, 16, v84
	s_mov_b64 exec, s[36:37]
	v_lshl_or_b32 v242, v91, 16, v90
	v_lshl_or_b32 v243, v93, 16, v92
	s_mov_b64 exec, -1
	s_waitcnt lgkmcnt(0)
	v_lshl_or_b32 v244, v99, 16, v98
	v_lshl_or_b32 v245, v101, 16, v100
	s_mov_b64 exec, s[36:37]
	v_lshl_or_b32 v246, v103, 16, v102
	v_lshl_or_b32 v247, v105, 16, v104
	s_mov_b64 exec, -1
	s_waitcnt lgkmcnt(0)
	s_mov_b64 exec, s[38:39]
	v_cvt_pk_bf16_f32 v66, v2, v195
	v_cvt_pk_bf16_f32 v74, v3, v195
	v_lshlrev_b32_e32 v67, 16, v66
	v_lshlrev_b32_e32 v75, 16, v74
	v_sub_f32_e32 v2, v2, v67
	v_sub_f32_e32 v3, v3, v75
	v_cvt_pk_bf16_f32 v68, v2, v195
	v_cvt_pk_bf16_f32 v76, v3, v195
	v_lshlrev_b32_e32 v69, 16, v68
	v_lshlrev_b32_e32 v77, 16, v76
	v_sub_f32_e32 v2, v2, v69
	v_sub_f32_e32 v3, v3, v77
	v_cvt_pk_bf16_f32 v147, v2, v195
	v_cvt_pk_bf16_f32 v151, v3, v195
	v_cvt_pk_bf16_f32 v146, v67, v69
	v_cvt_pk_bf16_f32 v150, v75, v77
	v_cvt_pk_bf16_f32 v66, v4, v195
	v_cvt_pk_bf16_f32 v74, v5, v195
	v_lshlrev_b32_e32 v67, 16, v66
	v_lshlrev_b32_e32 v75, 16, v74
	v_sub_f32_e32 v4, v4, v67
	v_sub_f32_e32 v5, v5, v75
	v_cvt_pk_bf16_f32 v68, v4, v195
	v_cvt_pk_bf16_f32 v76, v5, v195
	v_lshlrev_b32_e32 v69, 16, v68
	v_lshlrev_b32_e32 v77, 16, v76
	v_sub_f32_e32 v4, v4, v69
	v_sub_f32_e32 v5, v5, v77
	v_cvt_pk_bf16_f32 v155, v4, v195
	v_cvt_pk_bf16_f32 v159, v5, v195
	v_cvt_pk_bf16_f32 v154, v67, v69
	v_cvt_pk_bf16_f32 v158, v75, v77
	v_cvt_pk_bf16_f32 v66, v6, v195
	v_cvt_pk_bf16_f32 v74, v7, v195
	v_lshlrev_b32_e32 v67, 16, v66
	v_lshlrev_b32_e32 v75, 16, v74
	v_sub_f32_e32 v6, v6, v67
	v_sub_f32_e32 v7, v7, v75
	v_cvt_pk_bf16_f32 v68, v6, v195
	v_cvt_pk_bf16_f32 v76, v7, v195
	v_lshlrev_b32_e32 v69, 16, v68
	v_lshlrev_b32_e32 v77, 16, v76
	v_sub_f32_e32 v6, v6, v69
	v_sub_f32_e32 v7, v7, v77
	v_cvt_pk_bf16_f32 v163, v6, v195
	v_cvt_pk_bf16_f32 v167, v7, v195
	v_cvt_pk_bf16_f32 v162, v67, v69
	v_cvt_pk_bf16_f32 v166, v75, v77
	v_cvt_pk_bf16_f32 v66, v8, v195
	v_cvt_pk_bf16_f32 v74, v9, v195
	v_lshlrev_b32_e32 v67, 16, v66
	v_lshlrev_b32_e32 v75, 16, v74
	v_sub_f32_e32 v8, v8, v67
	v_sub_f32_e32 v9, v9, v75
	v_cvt_pk_bf16_f32 v68, v8, v195
	v_cvt_pk_bf16_f32 v76, v9, v195
	v_lshlrev_b32_e32 v69, 16, v68
	v_lshlrev_b32_e32 v77, 16, v76
	v_sub_f32_e32 v8, v8, v69
	v_sub_f32_e32 v9, v9, v77
	v_cvt_pk_bf16_f32 v171, v8, v195
	v_cvt_pk_bf16_f32 v175, v9, v195
	v_cvt_pk_bf16_f32 v170, v67, v69
	v_cvt_pk_bf16_f32 v174, v75, v77
	v_cvt_pk_bf16_f32 v66, v50, v195
	v_cvt_pk_bf16_f32 v74, v51, v195
	v_lshlrev_b32_e32 v67, 16, v66
	v_lshlrev_b32_e32 v75, 16, v74
	v_sub_f32_e32 v50, v50, v67
	v_sub_f32_e32 v51, v51, v75
	v_cvt_pk_bf16_f32 v68, v50, v195
	v_cvt_pk_bf16_f32 v76, v51, v195
	v_lshlrev_b32_e32 v69, 16, v68
	v_lshlrev_b32_e32 v77, 16, v76
	v_sub_f32_e32 v50, v50, v69
	v_sub_f32_e32 v51, v51, v77
	v_cvt_pk_bf16_f32 v179, v50, v195
	v_cvt_pk_bf16_f32 v183, v51, v195
	v_cvt_pk_bf16_f32 v178, v67, v69
	v_cvt_pk_bf16_f32 v182, v75, v77
	v_cvt_pk_bf16_f32 v66, v52, v195
	v_cvt_pk_bf16_f32 v74, v53, v195
	v_lshlrev_b32_e32 v67, 16, v66
	v_lshlrev_b32_e32 v75, 16, v74
	v_sub_f32_e32 v52, v52, v67
	v_sub_f32_e32 v53, v53, v75
	v_cvt_pk_bf16_f32 v68, v52, v195
	v_cvt_pk_bf16_f32 v76, v53, v195
	v_lshlrev_b32_e32 v69, 16, v68
	v_lshlrev_b32_e32 v77, 16, v76
	v_sub_f32_e32 v52, v52, v69
	v_sub_f32_e32 v53, v53, v77
	v_cvt_pk_bf16_f32 v187, v52, v195
	v_cvt_pk_bf16_f32 v191, v53, v195
	v_cvt_pk_bf16_f32 v186, v67, v69
	v_cvt_pk_bf16_f32 v190, v75, v77
	v_cvt_pk_bf16_f32 v66, v58, v195
	v_cvt_pk_bf16_f32 v74, v59, v195
	v_lshlrev_b32_e32 v67, 16, v66
	v_lshlrev_b32_e32 v75, 16, v74
	v_sub_f32_e32 v58, v58, v67
	v_sub_f32_e32 v59, v59, v75
	v_cvt_pk_bf16_f32 v68, v58, v195
	v_cvt_pk_bf16_f32 v76, v59, v195
	v_lshlrev_b32_e32 v69, 16, v68
	v_lshlrev_b32_e32 v77, 16, v76
	v_sub_f32_e32 v58, v58, v69
	v_sub_f32_e32 v59, v59, v77
	v_cvt_pk_bf16_f32 v235, v58, v195
	v_cvt_pk_bf16_f32 v239, v59, v195
	v_cvt_pk_bf16_f32 v234, v67, v69
	v_cvt_pk_bf16_f32 v238, v75, v77
	v_cvt_pk_bf16_f32 v66, v60, v195
	v_cvt_pk_bf16_f32 v74, v61, v195
	v_lshlrev_b32_e32 v67, 16, v66
	v_lshlrev_b32_e32 v75, 16, v74
	v_sub_f32_e32 v60, v60, v67
	v_sub_f32_e32 v61, v61, v75
	v_cvt_pk_bf16_f32 v68, v60, v195
	v_cvt_pk_bf16_f32 v76, v61, v195
	v_lshlrev_b32_e32 v69, 16, v68
	v_lshlrev_b32_e32 v77, 16, v76
	v_sub_f32_e32 v60, v60, v69
	v_sub_f32_e32 v61, v61, v77
	v_cvt_pk_bf16_f32 v243, v60, v195
	v_cvt_pk_bf16_f32 v247, v61, v195
	v_cvt_pk_bf16_f32 v242, v67, v69
	v_cvt_pk_bf16_f32 v246, v75, v77
	s_mov_b64 exec, -1
	s_waitcnt vmcnt(15)
	v_cvt_pk_bf16_f32 v6, v10, v11
	v_cvt_pk_bf16_f32 v7, v12, v13
	ds_write_b64 v212, v[6:7]
	s_waitcnt vmcnt(14)
	v_cvt_pk_bf16_f32 v6, v14, v15
	v_cvt_pk_bf16_f32 v7, v16, v17
	ds_write_b64 v211, v[6:7] offset:512
	s_waitcnt vmcnt(13)
	v_cvt_pk_bf16_f32 v6, v22, v23
	v_cvt_pk_bf16_f32 v7, v24, v25
	ds_write_b64 v210, v[6:7] offset:1024
	s_waitcnt vmcnt(12)
	v_cvt_pk_bf16_f32 v6, v30, v31
	v_cvt_pk_bf16_f32 v7, v32, v33
	ds_write_b64 v209, v[6:7] offset:1536
	s_waitcnt vmcnt(11)
	v_cvt_pk_bf16_f32 v6, v38, v39
	v_cvt_pk_bf16_f32 v7, v40, v41
	ds_write_b64 v208, v[6:7] offset:2048
	s_waitcnt vmcnt(10)
	v_cvt_pk_bf16_f32 v6, v46, v47
	v_cvt_pk_bf16_f32 v7, v48, v49
	ds_write_b64 v207, v[6:7] offset:2560
	s_waitcnt vmcnt(9)
	v_cvt_pk_bf16_f32 v6, v54, v55
	v_cvt_pk_bf16_f32 v7, v56, v57
	ds_write_b64 v206, v[6:7] offset:3072
	s_waitcnt vmcnt(8)
	v_cvt_pk_bf16_f32 v6, v62, v63
	v_cvt_pk_bf16_f32 v7, v64, v65
	ds_write_b64 v205, v[6:7] offset:3584
	s_waitcnt vmcnt(7)
	v_cvt_pk_bf16_f32 v6, v70, v71
	v_cvt_pk_bf16_f32 v7, v72, v73
	ds_write_b64 v231, v[6:7] offset:4096
	s_waitcnt vmcnt(6)
	v_cvt_pk_bf16_f32 v6, v78, v79
	v_cvt_pk_bf16_f32 v7, v80, v81
	ds_write_b64 v230, v[6:7] offset:4608
	s_waitcnt vmcnt(5)
	v_cvt_pk_bf16_f32 v6, v86, v87
	v_cvt_pk_bf16_f32 v7, v88, v89
	ds_write_b64 v229, v[6:7] offset:5120
	s_waitcnt vmcnt(4)
	v_cvt_pk_bf16_f32 v6, v94, v95
	v_cvt_pk_bf16_f32 v7, v96, v97
	ds_write_b64 v228, v[6:7] offset:5632
	s_waitcnt vmcnt(3)
	v_cvt_pk_bf16_f32 v6, v106, v107
	v_cvt_pk_bf16_f32 v7, v108, v109
	ds_write_b64 v227, v[6:7] offset:6144
	s_waitcnt vmcnt(2)
	v_cvt_pk_bf16_f32 v6, v114, v115
	v_cvt_pk_bf16_f32 v7, v116, v117
	ds_write_b64 v226, v[6:7] offset:6656
	s_waitcnt vmcnt(1)
	v_cvt_pk_bf16_f32 v6, v122, v123
	v_cvt_pk_bf16_f32 v7, v124, v125
	s_waitcnt lgkmcnt(14)
	v_mfma_f32_16x16x32_bf16 v[2:5], v[26:29], v[42:45], v[18:21]
	ds_write_b64 v225, v[6:7] offset:7168
	s_waitcnt vmcnt(0)
	v_cvt_pk_bf16_f32 v6, v130, v131
	v_cvt_pk_bf16_f32 v7, v132, v133
	ds_write_b64 v224, v[6:7] offset:7680
	v_lshlrev_b32_e32 v6, 3, v142
	v_and_b32_e32 v58, 56, v6
	v_lshl_or_b32 v6, v58, 10, v198
	v_or_b32_e32 v18, 1, v58
	v_lshl_or_b32 v7, v58, 8, v204
	ds_read_b128 v[14:17], v6
	ds_read_b128 v[10:13], v7
	v_lshl_or_b32 v6, v18, 10, v198
	ds_read_b128 v[26:29], v6
	ds_read_b128 v[22:25], v223
	ds_read_b128 v[6:9], v222
	v_or_b32_e32 v42, 2, v58
	v_lshl_or_b32 v19, v42, 10, v198
	ds_read_b128 v[38:41], v19
	s_waitcnt lgkmcnt(2)
	v_mfma_f32_16x16x32_bf16 v[30:33], v[14:17], v[22:25], v[34:37]
	v_lshl_or_b32 v14, v18, 8, v204
	ds_read_b128 v[18:21], v14
	ds_read_b128 v[14:17], v221
	v_or_b32_e32 v59, 5, v58
	s_waitcnt lgkmcnt(3)
	v_mfma_f32_16x16x32_bf16 v[34:37], v[26:29], v[6:9], v[30:33]
	v_lshl_or_b32 v26, v42, 8, v204
	ds_read_b128 v[26:29], v26
	s_nop 0
	ds_read_b128 v[30:33], v219
	v_or_b32_e32 v68, 6, v58
	s_waitcnt lgkmcnt(2)
	v_mfma_f32_16x16x32_bf16 v[38:41], v[38:41], v[14:17], v[34:37]
	v_lshl_or_b32 v64, v68, 10, v198
	s_nop 1
	v_or_b32_e32 v34, 3, v58
	v_lshl_or_b32 v35, v34, 10, v198
	ds_read_b128 v[42:45], v35
	v_lshl_or_b32 v34, v34, 8, v204
	s_waitcnt lgkmcnt(0)
	v_mfma_f32_16x16x32_bf16 v[46:49], v[42:45], v[30:33], v[38:41]
	s_nop 2
	v_or_b32_e32 v38, 4, v58
	v_lshl_or_b32 v39, v38, 10, v198
	v_lshl_or_b32 v38, v38, 8, v204
	ds_read_b128 v[34:37], v34
	ds_read_b128 v[50:53], v39
	ds_read_b128 v[42:45], v38
	v_lshl_or_b32 v38, v59, 10, v198
	ds_read_b128 v[54:57], v38
	ds_read_b128 v[60:63], v218
	ds_read_b128 v[38:41], v217
	ds_read_b128 v[72:75], v64
	s_waitcnt lgkmcnt(2)
	v_mfma_f32_16x16x32_bf16 v[64:67], v[50:53], v[60:63], v[46:49]
	v_or_b32_e32 v58, 7, v58
	s_nop 1
	v_lshl_or_b32 v46, v59, 8, v204
	v_lshl_or_b32 v59, v68, 8, v204
	ds_read_b128 v[50:53], v46
	ds_read_b128 v[46:49], v216
	s_waitcnt lgkmcnt(3)
	v_mfma_f32_16x16x32_bf16 v[54:57], v[54:57], v[38:41], v[64:67]
	s_nop 2
	ds_read_b128 v[64:67], v59
	ds_read_b128 v[68:71], v213
	v_lshl_or_b32 v59, v58, 10, v198
	ds_read_b128 v[76:79], v59
	s_waitcnt lgkmcnt(3)
	v_mfma_f32_16x16x32_bf16 v[54:57], v[72:75], v[46:49], v[54:57]
	v_lshl_or_b32 v58, v58, 8, v204
	ds_read_b128 v[72:75], v58
	s_waitcnt lgkmcnt(1)
	v_mfma_f32_16x16x32_bf16 v[56:59], v[76:79], v[68:71], v[54:57]
	s_nop 2
	v_add_u32_e32 v76, 0x24800, v196
	s_waitcnt lgkmcnt(0)
	v_mfma_f32_16x16x32_bf16 v[2:5], v[10:13], v[22:25], v[2:5]
	v_mfma_f32_16x16x32_bf16 v[2:5], v[18:21], v[6:9], v[2:5]
	s_waitcnt lgkmcnt(0)
	v_mfma_f32_16x16x32_bf16 v[2:5], v[26:29], v[14:17], v[2:5]
	v_mfma_f32_16x16x32_bf16 v[2:5], v[34:37], v[30:33], v[2:5]
	s_waitcnt lgkmcnt(0)
	v_mfma_f32_16x16x32_bf16 v[2:5], v[42:45], v[60:63], v[2:5]
	v_mfma_f32_16x16x32_bf16 v[2:5], v[50:53], v[38:41], v[2:5]
	s_waitcnt lgkmcnt(0)
	v_mfma_f32_16x16x32_bf16 v[2:5], v[64:67], v[46:49], v[2:5]
	v_mfma_f32_16x16x32_bf16 v[60:63], v[72:75], v[68:71], v[2:5]
	s_waitcnt lgkmcnt(0)
	v_cmp_gt_u32_e64 s[0:1], 16, v1
	v_cmp_lt_u32_e32 vcc, 15, v1
	s_waitcnt lgkmcnt(0)
	s_nop 2
	v_max_f32_e32 v2, v59, v59
	v_max_f32_e32 v3, v58, v58
	s_waitcnt lgkmcnt(0)
	v_max_f32_e32 v2, v3, v2
	s_nop 0
	s_nop 0
	s_nop 0
	s_waitcnt lgkmcnt(0)
	s_nop 0
	s_nop 0
	s_and_saveexec_b64 s[4:5], vcc
	s_xor_b64 s[4:5], exec, s[4:5]
	s_or_saveexec_b64 s[4:5], s[4:5]
	v_max3_f32 v53, v56, v57, v2
	s_xor_b64 exec, exec, s[4:5]
	v_max_f32_e32 v2, v61, v61
	v_max_f32_e32 v3, v60, v60
	v_max_f32_e32 v2, v3, v2
	v_max_f32_e32 v3, v63, v63
	v_max_f32_e32 v4, v62, v62
	v_max_f32_e32 v3, v4, v3
	v_max3_f32 v53, v53, v2, v3
	s_or_b64 exec, exec, s[4:5]
	v_cmp_eq_u32_e64 s[4:5], 1, v201
	v_max_f32_e32 v53, v53, v53
	v_mov_b32_e32 v68, v53
	s_nop 1
	v_permlane16_swap_b32_e32 v53, v68
	v_max_f32_e32 v68, v53, v68
	v_mov_b32_e32 v55, v68
	s_nop 1
	v_permlane32_swap_b32_e32 v68, v55
	v_max_f32_e32 v68, v68, v55
	v_sub_f32_e32 v55, v56, v68
	v_mul_f32_e32 v55, 0x3fb8aa3b, v55
	v_exp_f32_e32 v70, v55
	v_sub_f32_e32 v55, v57, v68
	v_sub_f32_e32 v57, v59, v68
	v_mul_f32_e32 v57, 0x3fb8aa3b, v57
	v_mul_f32_e32 v55, 0x3fb8aa3b, v55
	v_exp_f32_e32 v59, v57
	v_sub_f32_e32 v57, v60, v68
	v_exp_f32_e32 v71, v55
	v_sub_f32_e32 v55, v58, v68
	v_mul_f32_e32 v57, 0x3fb8aa3b, v57
	v_sub_f32_e32 v58, v61, v68
	v_exp_f32_e32 v57, v57
	v_mul_f32_e32 v58, 0x3fb8aa3b, v58
	v_exp_f32_e32 v58, v58
	v_mul_f32_e32 v55, 0x3fb8aa3b, v55
	v_exp_f32_e32 v72, v55
	v_cndmask_b32_e64 v60, 0, v57, s[0:1]
	v_sub_f32_e32 v57, v62, v68
	v_add_f32_e32 v56, 0, v70
	v_cndmask_b32_e64 v61, 0, v58, s[0:1]
	v_mul_f32_e32 v57, 0x3fb8aa3b, v57
	v_sub_f32_e32 v58, v63, v68
	v_add_f32_e32 v56, v56, v71
	v_exp_f32_e32 v57, v57
	v_mul_f32_e32 v58, 0x3fb8aa3b, v58
	v_add_f32_e32 v56, v56, v72
	v_exp_f32_e32 v58, v58
	v_add_f32_e32 v56, v56, v59
	v_add_f32_e32 v56, v56, v60
	v_add_f32_e32 v56, v56, v61
	v_cndmask_b32_e64 v62, 0, v57, s[0:1]
	v_add_f32_e32 v56, v56, v62
	v_cndmask_b32_e64 v63, 0, v58, s[0:1]
	v_add_f32_e32 v57, v56, v63
	v_mov_b32_e32 v58, v57
	s_nop 1
	v_permlane16_swap_b32_e32 v57, v58
	v_add_f32_e32 v58, v57, v58
	v_mov_b32_e32 v68, v58
	s_nop 1
	v_permlane32_swap_b32_e32 v58, v68
	v_add_f32_e32 v68, v58, v68
	v_div_scale_f32 v69, s[6:7], v68, v68, 1.0
	v_rcp_f32_e32 v73, v69
	s_nop 0
	v_fma_f32 v75, -v69, v73, 1.0
	v_fmac_f32_e32 v73, v75, v73
	v_div_scale_f32 v75, vcc, 1.0, v68, 1.0
	v_mul_f32_e32 v92, v75, v73
	v_fma_f32 v93, -v69, v92, v75
	v_fmac_f32_e32 v92, v93, v73
	v_fma_f32 v69, -v69, v92, v75
	v_div_fmas_f32 v69, v69, v73, v92
	v_div_fixup_f32 v68, v69, v68, 1.0
	v_mul_f32_e32 v69, v68, v70
	v_mov_b32_e32 v75, 0xbb23d70a
	v_mov_b32_e32 v73, 0x3b23d70a
	v_fmaak_f32 v92, v68, v70, 0xbb23d70a
	v_fmaak_f32 v70, v68, v70, 0x3b23d70a
	v_cmp_lt_f32_e32 vcc, v69, v75
	v_fmaak_f32 v93, v68, v60, 0xbb23d70a
	s_nop 0
	v_cndmask_b32_e32 v70, 0, v70, vcc
	v_cmp_gt_f32_e32 vcc, v69, v73
	s_nop 1
	v_cndmask_b32_e32 v69, v70, v92, vcc
	v_mul_f32_e32 v92, v68, v60
	v_fmaak_f32 v60, v68, v60, 0x3b23d70a
	v_cmp_lt_f32_e32 vcc, v92, v75
	v_max_f32_e32 v70, 0xf149f2ca, v69
	s_nop 0
	v_cndmask_b32_e32 v60, 0, v60, vcc
	v_cmp_gt_f32_e32 vcc, v92, v73
	s_nop 1
	v_cndmask_b32_e32 v92, v60, v93, vcc
	v_max_f32_e32 v60, v70, v92
	v_cndmask_b32_e64 v60, v70, v60, s[0:1]
	v_mul_f32_e32 v70, v68, v71
	v_fmaak_f32 v93, v68, v71, 0xbb23d70a
	v_fmaak_f32 v71, v68, v71, 0x3b23d70a
	v_cmp_lt_f32_e32 vcc, v70, v75
	s_nop 1
	v_cndmask_b32_e32 v71, 0, v71, vcc
	v_cmp_gt_f32_e32 vcc, v70, v73
	s_nop 1
	v_cndmask_b32_e32 v70, v71, v93, vcc
	v_mul_f32_e32 v71, v68, v61
	v_fmaak_f32 v93, v68, v61, 0xbb23d70a
	v_fmaak_f32 v61, v68, v61, 0x3b23d70a
	v_cmp_lt_f32_e32 vcc, v71, v75
	v_max_f32_e32 v60, v60, v70
	s_nop 0
	v_cndmask_b32_e32 v61, 0, v61, vcc
	v_cmp_gt_f32_e32 vcc, v71, v73
	s_nop 1
	v_cndmask_b32_e32 v71, v61, v93, vcc
	v_max_f32_e32 v61, v60, v71
	v_cndmask_b32_e64 v60, v60, v61, s[0:1]
	v_mul_f32_e32 v61, v68, v72
	v_fmaak_f32 v93, v68, v72, 0xbb23d70a
	v_fmaak_f32 v72, v68, v72, 0x3b23d70a
	v_cmp_lt_f32_e32 vcc, v61, v75
	s_nop 1
	v_cndmask_b32_e32 v72, 0, v72, vcc
	v_cmp_gt_f32_e32 vcc, v61, v73
	v_mul_f32_e32 v61, v68, v62
	s_nop 0
	v_cndmask_b32_e32 v72, v72, v93, vcc
	v_fmaak_f32 v93, v68, v62, 0xbb23d70a
	v_fmaak_f32 v62, v68, v62, 0x3b23d70a
	v_cmp_lt_f32_e32 vcc, v61, v75
	v_max_f32_e32 v60, v60, v72
	s_nop 0
	v_cndmask_b32_e32 v62, 0, v62, vcc
	v_cmp_gt_f32_e32 vcc, v61, v73
	s_nop 1
	v_cndmask_b32_e32 v62, v62, v93, vcc
	v_max_f32_e32 v61, v60, v62
	v_cndmask_b32_e64 v60, v60, v61, s[0:1]
	v_mul_f32_e32 v61, v68, v59
	v_fmaak_f32 v93, v68, v59, 0xbb23d70a
	v_fmaak_f32 v59, v68, v59, 0x3b23d70a
	v_cmp_lt_f32_e32 vcc, v61, v75
	s_nop 1
	v_cndmask_b32_e32 v59, 0, v59, vcc
	v_cmp_gt_f32_e32 vcc, v61, v73
	s_nop 1
	v_cndmask_b32_e32 v93, v59, v93, vcc
	v_max_f32_e32 v59, v60, v93
	v_mul_f32_e32 v60, v68, v63
	v_cmp_gt_f32_e32 vcc, v60, v73
	v_fmac_f32_e32 v73, v68, v63
	v_cmp_lt_f32_e64 s[6:7], v60, v75
	v_fmac_f32_e32 v75, v68, v63
	s_nop 0
	v_cndmask_b32_e64 v60, 0, v73, s[6:7]
	v_cndmask_b32_e32 v63, v60, v75, vcc
	v_max_f32_e32 v60, v59, v63
	v_cndmask_b32_e64 v60, v59, v60, s[0:1]
	v_mov_b32_e32 v61, v60
	s_nop 1
	v_permlane16_swap_b32_e32 v60, v61
	v_max_f32_e32 v61, v60, v61
	v_mov_b32_e32 v74, v61
	s_nop 1
	v_permlane32_swap_b32_e32 v61, v74
	v_max_f32_e32 v74, v61, v74
	v_sub_f32_e32 v61, v69, v74
	v_mul_f32_e32 v61, 0x3fb8aa3b, v61
	v_exp_f32_e32 v69, v61
	v_sub_f32_e32 v61, v92, v74
	v_mul_f32_e32 v61, 0x3fb8aa3b, v61
	v_exp_f32_e32 v75, v61
	v_sub_f32_e32 v70, v70, v74
	v_sub_f32_e32 v71, v71, v74
	v_mul_f32_e32 v70, 0x3fb8aa3b, v70
	v_mul_f32_e32 v71, 0x3fb8aa3b, v71
	v_exp_f32_e32 v70, v70
	v_exp_f32_e32 v71, v71
	v_sub_f32_e32 v72, v72, v74
	v_sub_f32_e32 v62, v62, v74
	v_mul_f32_e32 v72, 0x3fb8aa3b, v72
	v_mul_f32_e32 v62, 0x3fb8aa3b, v62
	v_add_f32_e32 v73, 0, v69
	v_cndmask_b32_e64 v75, 0, v75, s[0:1]
	v_exp_f32_e32 v72, v72
	v_exp_f32_e32 v62, v62
	v_sub_f32_e32 v84, v93, v74
	v_sub_f32_e32 v63, v63, v74
	v_add_f32_e32 v73, v73, v75
	v_mul_f32_e32 v84, 0x3fb8aa3b, v84
	v_mul_f32_e32 v63, 0x3fb8aa3b, v63
	v_add_f32_e32 v73, v73, v70
	v_cndmask_b32_e64 v71, 0, v71, s[0:1]
	v_exp_f32_e32 v84, v84
	v_exp_f32_e32 v63, v63
	v_add_f32_e32 v73, v73, v71
	v_add_f32_e32 v73, v73, v72
	v_cndmask_b32_e64 v74, 0, v62, s[0:1]
	v_add_f32_e32 v62, v73, v74
	v_add_f32_e32 v62, v62, v84
	v_cndmask_b32_e64 v73, 0, v63, s[0:1]
	v_add_f32_e32 v85, v62, v73
	v_mov_b32_e32 v66, v85
	s_nop 1
	v_permlane16_swap_b32_e32 v85, v66
	v_add_f32_e32 v66, v85, v66
	v_mov_b32_e32 v67, v66
	s_nop 1
	v_permlane32_swap_b32_e32 v66, v67
	v_add_f32_e32 v66, v66, v67
	v_div_scale_f32 v67, s[6:7], v66, v66, 1.0
	v_rcp_f32_e32 v78, v67
	s_nop 0
	v_fma_f32 v68, -v67, v78, 1.0
	v_fmac_f32_e32 v78, v68, v78
	v_div_scale_f32 v68, vcc, 1.0, v66, 1.0
	v_mul_f32_e32 v77, v68, v78
	v_fma_f32 v79, -v67, v77, v68
	v_fmac_f32_e32 v77, v79, v78
	v_fma_f32 v67, -v67, v77, v68
	v_div_fmas_f32 v67, v67, v78, v77
	v_div_fixup_f32 v66, v67, v66, 1.0
	v_mov_b32_e32 v67, 0xbd4ccccd
	v_fmaak_f32 v68, v66, v69, 0xbd4ccccd
	v_fmaak_f32 v69, v66, v70, 0xbd4ccccd
	v_fmaak_f32 v70, v66, v72, 0xbd4ccccd
	v_fmaak_f32 v75, v66, v75, 0xbd4ccccd
	v_fmaak_f32 v71, v66, v71, 0xbd4ccccd
	v_fmaak_f32 v74, v66, v74, 0xbd4ccccd
	v_mul_f32_e32 v70, 0x4038aa3b, v70
	v_fmaak_f32 v72, v66, v84, 0xbd4ccccd
	v_mul_f32_e32 v75, 0x4038aa3b, v75
	v_mul_f32_e32 v71, 0x4038aa3b, v71
	v_mul_f32_e32 v74, 0x4038aa3b, v74
	v_fmac_f32_e32 v67, v66, v73
	v_mul_f32_e32 v68, 0x4038aa3b, v68
	v_mul_f32_e32 v69, 0x4038aa3b, v69
	v_mul_f32_e32 v72, 0x4038aa3b, v72
	v_cndmask_b32_e64 v75, 0, v75, s[0:1]
	v_cndmask_b32_e64 v71, 0, v71, s[0:1]
	v_cndmask_b32_e64 v74, 0, v74, s[0:1]
	v_mul_f32_e32 v66, 0x4038aa3b, v67
	v_cvt_pk_bf16_f32 v67, v70, v72
	v_add_u32_e32 v70, v76, v198
	v_cndmask_b32_e64 v73, 0, v66, s[0:1]
	v_cndmask_b32_e64 v74, v74, 1.0, s[4:5]
	v_cndmask_b32_e64 v75, v75, 1.0, s[4:5]
	v_cndmask_b32_e64 v71, v71, 1.0, s[4:5]
	v_cvt_pk_bf16_f32 v66, v68, v69
	v_cvt_pk_bf16_f32 v68, v75, v71
	v_cvt_pk_bf16_f32 v69, v74, v73
	ds_write_b128 v70, v[66:69]
	s_movk_i32 s0, 0x210
	v_and_b32_e32 v67, 48, v0
	v_lshrrev_b32_e32 v0, 5, v1
	v_mad_u32_u24 v66, v197, s0, v199
	v_mad_u32_u24 v68, v0, s0, v199
	s_and_b32 s0, s2, 7
	s_lshl_b32 s0, s0, 22
	s_lshl_b32 s1, s3, 17
	v_lshlrev_b32_e32 v1, 13, v0
	s_add_i32 s0, s0, s1
	v_and_b32_e32 v69, 0x1f0, v194
	v_or3_b32 v1, s0, v1, v196
	s_mov_b32 s12, 0
	s_mov_b32 s11, 0x20000
	s_brev_b32 s10, 8
	s_and_b32 s9, s9, 0xffff
	v_or_b32_e32 v0, 0x24800, v198
	v_add_u32_e32 v1, v1, v69
	v_add_u32_e32 v106, v66, v67
	v_add_u32_e32 v107, v68, v69
	s_waitcnt lgkmcnt(0)
	s_barrier
	ds_read_b128 v[70:73], v0
	v_add_u32_e32 v132, s12, v1
	s_add_i32 s12, s12, 0x2000000
	v_add_u32_e32 v0, 0x400, v0
	v_add_u32_e32 v133, 0x4000, v132
	v_add_u32_e32 v134, 0x8000, v132
	v_add_u32_e32 v135, 0xc000, v132
	v_add_u32_e32 v136, 0x10000, v132
	v_add_u32_e32 v137, 0x14000, v132
	v_add_u32_e32 v138, 0x18000, v132
	v_add_u32_e32 v139, 0x1c000, v132
	s_waitcnt lgkmcnt(0)
	v_mfma_f32_16x16x32_bf16 v[74:77], v[144:147], v[70:73], 0
	v_mfma_f32_16x16x32_bf16 v[78:81], v[148:151], v[70:73], 0
	v_mfma_f32_16x16x32_bf16 v[82:85], v[152:155], v[70:73], 0
	v_mfma_f32_16x16x32_bf16 v[86:89], v[156:159], v[70:73], 0
	v_mfma_f32_16x16x32_bf16 v[90:93], v[160:163], v[70:73], 0
	v_mfma_f32_16x16x32_bf16 v[94:97], v[164:167], v[70:73], 0
	v_mfma_f32_16x16x32_bf16 v[98:101], v[168:171], v[70:73], 0
	v_mfma_f32_16x16x32_bf16 v[102:105], v[172:175], v[70:73], 0
	s_nop 0
	v_exp_f32_e32 v74, v74
	v_exp_f32_e32 v75, v75
	v_exp_f32_e32 v76, v76
	v_exp_f32_e32 v77, v77
	v_exp_f32_e32 v78, v78
	v_exp_f32_e32 v79, v79
	v_exp_f32_e32 v80, v80
	v_exp_f32_e32 v81, v81
	v_exp_f32_e32 v82, v82
	v_exp_f32_e32 v83, v83
	v_exp_f32_e32 v84, v84
	v_exp_f32_e32 v85, v85
	v_exp_f32_e32 v86, v86
	v_exp_f32_e32 v87, v87
	v_exp_f32_e32 v88, v88
	v_exp_f32_e32 v89, v89
	v_exp_f32_e32 v90, v90
	v_exp_f32_e32 v91, v91
	v_exp_f32_e32 v92, v92
	v_exp_f32_e32 v93, v93
	v_exp_f32_e32 v94, v94
	v_exp_f32_e32 v95, v95
	v_exp_f32_e32 v96, v96
	v_exp_f32_e32 v97, v97
	v_exp_f32_e32 v98, v98
	v_exp_f32_e32 v99, v99
	v_exp_f32_e32 v100, v100
	v_exp_f32_e32 v101, v101
	v_exp_f32_e32 v102, v102
	v_exp_f32_e32 v103, v103
	v_exp_f32_e32 v104, v104
	v_exp_f32_e32 v105, v105
	v_add_f32_e32 v74, 1.0, v74
	v_add_f32_e32 v75, 1.0, v75
	v_add_f32_e32 v76, 1.0, v76
	v_add_f32_e32 v77, 1.0, v77
	v_add_f32_e32 v78, 1.0, v78
	v_add_f32_e32 v79, 1.0, v79
	v_add_f32_e32 v80, 1.0, v80
	v_add_f32_e32 v81, 1.0, v81
	v_add_f32_e32 v82, 1.0, v82
	v_add_f32_e32 v83, 1.0, v83
	v_add_f32_e32 v84, 1.0, v84
	v_add_f32_e32 v85, 1.0, v85
	v_add_f32_e32 v86, 1.0, v86
	v_add_f32_e32 v87, 1.0, v87
	v_add_f32_e32 v88, 1.0, v88
	v_add_f32_e32 v89, 1.0, v89
	v_add_f32_e32 v90, 1.0, v90
	v_add_f32_e32 v91, 1.0, v91
	v_add_f32_e32 v92, 1.0, v92
	v_add_f32_e32 v93, 1.0, v93
	v_add_f32_e32 v94, 1.0, v94
	v_add_f32_e32 v95, 1.0, v95
	v_add_f32_e32 v96, 1.0, v96
	v_add_f32_e32 v97, 1.0, v97
	v_add_f32_e32 v98, 1.0, v98
	v_add_f32_e32 v99, 1.0, v99
	v_add_f32_e32 v100, 1.0, v100
	v_add_f32_e32 v101, 1.0, v101
	v_add_f32_e32 v102, 1.0, v102
	v_add_f32_e32 v103, 1.0, v103
	v_add_f32_e32 v104, 1.0, v104
	v_add_f32_e32 v105, 1.0, v105
	v_rcp_f32_e32 v74, v74
	v_rcp_f32_e32 v75, v75
	v_rcp_f32_e32 v76, v76
	v_rcp_f32_e32 v77, v77
	v_rcp_f32_e32 v78, v78
	v_rcp_f32_e32 v79, v79
	v_rcp_f32_e32 v80, v80
	v_rcp_f32_e32 v81, v81
	v_rcp_f32_e32 v82, v82
	v_rcp_f32_e32 v83, v83
	v_rcp_f32_e32 v84, v84
	v_rcp_f32_e32 v85, v85
	v_rcp_f32_e32 v86, v86
	v_rcp_f32_e32 v87, v87
	v_rcp_f32_e32 v88, v88
	v_rcp_f32_e32 v89, v89
	v_rcp_f32_e32 v90, v90
	v_rcp_f32_e32 v91, v91
	v_rcp_f32_e32 v92, v92
	v_rcp_f32_e32 v93, v93
	v_rcp_f32_e32 v94, v94
	v_rcp_f32_e32 v95, v95
	v_rcp_f32_e32 v96, v96
	v_rcp_f32_e32 v97, v97
	v_rcp_f32_e32 v98, v98
	v_rcp_f32_e32 v99, v99
	v_rcp_f32_e32 v100, v100
	v_rcp_f32_e32 v101, v101
	v_rcp_f32_e32 v102, v102
	v_rcp_f32_e32 v103, v103
	v_rcp_f32_e32 v104, v104
	v_rcp_f32_e32 v105, v105
	v_pk_fma_f32 v[74:75], v[74:75], -2.0, 1.0 op_sel_hi:[1,0,0]
	v_pk_fma_f32 v[76:77], v[76:77], -2.0, 1.0 op_sel_hi:[1,0,0]
	v_pk_fma_f32 v[78:79], v[78:79], -2.0, 1.0 op_sel_hi:[1,0,0]
	v_pk_fma_f32 v[80:81], v[80:81], -2.0, 1.0 op_sel_hi:[1,0,0]
	v_pk_fma_f32 v[82:83], v[82:83], -2.0, 1.0 op_sel_hi:[1,0,0]
	v_pk_fma_f32 v[84:85], v[84:85], -2.0, 1.0 op_sel_hi:[1,0,0]
	v_pk_fma_f32 v[86:87], v[86:87], -2.0, 1.0 op_sel_hi:[1,0,0]
	v_pk_fma_f32 v[88:89], v[88:89], -2.0, 1.0 op_sel_hi:[1,0,0]
	v_pk_fma_f32 v[90:91], v[90:91], -2.0, 1.0 op_sel_hi:[1,0,0]
	v_pk_fma_f32 v[92:93], v[92:93], -2.0, 1.0 op_sel_hi:[1,0,0]
	v_pk_fma_f32 v[94:95], v[94:95], -2.0, 1.0 op_sel_hi:[1,0,0]
	v_pk_fma_f32 v[96:97], v[96:97], -2.0, 1.0 op_sel_hi:[1,0,0]
	v_pk_fma_f32 v[98:99], v[98:99], -2.0, 1.0 op_sel_hi:[1,0,0]
	v_pk_fma_f32 v[100:101], v[100:101], -2.0, 1.0 op_sel_hi:[1,0,0]
	v_pk_fma_f32 v[102:103], v[102:103], -2.0, 1.0 op_sel_hi:[1,0,0]
	v_pk_fma_f32 v[104:105], v[104:105], -2.0, 1.0 op_sel_hi:[1,0,0]
	ds_write_b128 v106, v[74:77]
	ds_write_b128 v106, v[78:81] offset:64
	ds_write_b128 v106, v[82:85] offset:128
	ds_write_b128 v106, v[86:89] offset:192
	ds_write_b128 v106, v[90:93] offset:256
	ds_write_b128 v106, v[94:97] offset:320
	ds_write_b128 v106, v[98:101] offset:384
	ds_write_b128 v106, v[102:105] offset:448
	ds_read_b128 v[74:77], v107
	ds_read_b128 v[78:81], v107 offset:1056
	ds_read_b128 v[82:85], v107 offset:2112
	ds_read_b128 v[86:89], v107 offset:3168
	ds_read_b128 v[90:93], v107 offset:4224
	ds_read_b128 v[94:97], v107 offset:5280
	ds_read_b128 v[98:101], v107 offset:6336
	ds_read_b128 v[102:105], v107 offset:7392
	s_waitcnt lgkmcnt(7)
	buffer_store_dwordx4 v[74:77], v132, s[8:11], 0 offen sc0 nt sc1
	s_waitcnt lgkmcnt(6)
	buffer_store_dwordx4 v[78:81], v133, s[8:11], 0 offen sc0 nt sc1
	s_waitcnt lgkmcnt(5)
	buffer_store_dwordx4 v[82:85], v134, s[8:11], 0 offen sc0 nt sc1
	s_waitcnt lgkmcnt(4)
	buffer_store_dwordx4 v[86:89], v135, s[8:11], 0 offen sc0 nt sc1
	s_waitcnt lgkmcnt(3)
	buffer_store_dwordx4 v[90:93], v136, s[8:11], 0 offen sc0 nt sc1
	s_waitcnt lgkmcnt(2)
	buffer_store_dwordx4 v[94:97], v137, s[8:11], 0 offen sc0 nt sc1
	s_waitcnt lgkmcnt(1)
	buffer_store_dwordx4 v[98:101], v138, s[8:11], 0 offen sc0 nt sc1
	s_waitcnt lgkmcnt(0)
	buffer_store_dwordx4 v[102:105], v139, s[8:11], 0 offen sc0 nt sc1
	v_mfma_f32_16x16x32_bf16 v[74:77], v[176:179], v[70:73], 0
	v_mfma_f32_16x16x32_bf16 v[78:81], v[180:183], v[70:73], 0
	v_mfma_f32_16x16x32_bf16 v[82:85], v[184:187], v[70:73], 0
	v_mfma_f32_16x16x32_bf16 v[86:89], v[188:191], v[70:73], 0
	v_mfma_f32_16x16x32_bf16 v[90:93], v[232:235], v[70:73], 0
	v_mfma_f32_16x16x32_bf16 v[94:97], v[236:239], v[70:73], 0
	v_mfma_f32_16x16x32_bf16 v[98:101], v[240:243], v[70:73], 0
	v_mfma_f32_16x16x32_bf16 v[102:105], v[244:247], v[70:73], 0
	s_nop 0
	v_exp_f32_e32 v74, v74
	v_exp_f32_e32 v75, v75
	v_exp_f32_e32 v76, v76
	v_exp_f32_e32 v77, v77
	v_exp_f32_e32 v78, v78
	v_exp_f32_e32 v79, v79
	v_exp_f32_e32 v80, v80
	v_exp_f32_e32 v81, v81
	v_exp_f32_e32 v82, v82
	v_exp_f32_e32 v83, v83
	v_exp_f32_e32 v84, v84
	v_exp_f32_e32 v85, v85
	v_exp_f32_e32 v86, v86
	v_exp_f32_e32 v87, v87
	v_exp_f32_e32 v88, v88
	v_exp_f32_e32 v89, v89
	v_exp_f32_e32 v90, v90
	v_exp_f32_e32 v91, v91
	v_exp_f32_e32 v92, v92
	v_exp_f32_e32 v93, v93
	v_exp_f32_e32 v94, v94
	v_exp_f32_e32 v95, v95
	v_exp_f32_e32 v96, v96
	v_exp_f32_e32 v97, v97
	v_exp_f32_e32 v98, v98
	v_exp_f32_e32 v99, v99
	v_exp_f32_e32 v100, v100
	v_exp_f32_e32 v101, v101
	v_exp_f32_e32 v102, v102
	v_exp_f32_e32 v103, v103
	v_exp_f32_e32 v104, v104
	v_exp_f32_e32 v105, v105
	v_add_f32_e32 v74, 1.0, v74
	v_add_f32_e32 v75, 1.0, v75
	v_add_f32_e32 v76, 1.0, v76
	v_add_f32_e32 v77, 1.0, v77
	v_add_f32_e32 v78, 1.0, v78
	v_add_f32_e32 v79, 1.0, v79
	v_add_f32_e32 v80, 1.0, v80
	v_add_f32_e32 v81, 1.0, v81
	v_add_f32_e32 v82, 1.0, v82
	v_add_f32_e32 v83, 1.0, v83
	v_add_f32_e32 v84, 1.0, v84
	v_add_f32_e32 v85, 1.0, v85
	v_add_f32_e32 v86, 1.0, v86
	v_add_f32_e32 v87, 1.0, v87
	v_add_f32_e32 v88, 1.0, v88
	v_add_f32_e32 v89, 1.0, v89
	v_add_f32_e32 v90, 1.0, v90
	v_add_f32_e32 v91, 1.0, v91
	v_add_f32_e32 v92, 1.0, v92
	v_add_f32_e32 v93, 1.0, v93
	v_add_f32_e32 v94, 1.0, v94
	v_add_f32_e32 v95, 1.0, v95
	v_add_f32_e32 v96, 1.0, v96
	v_add_f32_e32 v97, 1.0, v97
	v_add_f32_e32 v98, 1.0, v98
	v_add_f32_e32 v99, 1.0, v99
	v_add_f32_e32 v100, 1.0, v100
	v_add_f32_e32 v101, 1.0, v101
	v_add_f32_e32 v102, 1.0, v102
	v_add_f32_e32 v103, 1.0, v103
	v_add_f32_e32 v104, 1.0, v104
	v_add_f32_e32 v105, 1.0, v105
	v_rcp_f32_e32 v74, v74
	v_rcp_f32_e32 v75, v75
	v_rcp_f32_e32 v76, v76
	v_rcp_f32_e32 v77, v77
	v_rcp_f32_e32 v78, v78
	v_rcp_f32_e32 v79, v79
	v_rcp_f32_e32 v80, v80
	v_rcp_f32_e32 v81, v81
	v_rcp_f32_e32 v82, v82
	v_rcp_f32_e32 v83, v83
	v_rcp_f32_e32 v84, v84
	v_rcp_f32_e32 v85, v85
	v_rcp_f32_e32 v86, v86
	v_rcp_f32_e32 v87, v87
	v_rcp_f32_e32 v88, v88
	v_rcp_f32_e32 v89, v89
	v_rcp_f32_e32 v90, v90
	v_rcp_f32_e32 v91, v91
	v_rcp_f32_e32 v92, v92
	v_rcp_f32_e32 v93, v93
	v_rcp_f32_e32 v94, v94
	v_rcp_f32_e32 v95, v95
	v_rcp_f32_e32 v96, v96
	v_rcp_f32_e32 v97, v97
	v_rcp_f32_e32 v98, v98
	v_rcp_f32_e32 v99, v99
	v_rcp_f32_e32 v100, v100
	v_rcp_f32_e32 v101, v101
	v_rcp_f32_e32 v102, v102
	v_rcp_f32_e32 v103, v103
	v_rcp_f32_e32 v104, v104
	v_rcp_f32_e32 v105, v105
	v_pk_fma_f32 v[74:75], v[74:75], -2.0, 1.0 op_sel_hi:[1,0,0]
	v_pk_fma_f32 v[76:77], v[76:77], -2.0, 1.0 op_sel_hi:[1,0,0]
	v_pk_fma_f32 v[78:79], v[78:79], -2.0, 1.0 op_sel_hi:[1,0,0]
	v_pk_fma_f32 v[80:81], v[80:81], -2.0, 1.0 op_sel_hi:[1,0,0]
	v_pk_fma_f32 v[82:83], v[82:83], -2.0, 1.0 op_sel_hi:[1,0,0]
	v_pk_fma_f32 v[84:85], v[84:85], -2.0, 1.0 op_sel_hi:[1,0,0]
	v_pk_fma_f32 v[86:87], v[86:87], -2.0, 1.0 op_sel_hi:[1,0,0]
	v_pk_fma_f32 v[88:89], v[88:89], -2.0, 1.0 op_sel_hi:[1,0,0]
	v_pk_fma_f32 v[90:91], v[90:91], -2.0, 1.0 op_sel_hi:[1,0,0]
	v_pk_fma_f32 v[92:93], v[92:93], -2.0, 1.0 op_sel_hi:[1,0,0]
	v_pk_fma_f32 v[94:95], v[94:95], -2.0, 1.0 op_sel_hi:[1,0,0]
	v_pk_fma_f32 v[96:97], v[96:97], -2.0, 1.0 op_sel_hi:[1,0,0]
	v_pk_fma_f32 v[98:99], v[98:99], -2.0, 1.0 op_sel_hi:[1,0,0]
	v_pk_fma_f32 v[100:101], v[100:101], -2.0, 1.0 op_sel_hi:[1,0,0]
	v_pk_fma_f32 v[102:103], v[102:103], -2.0, 1.0 op_sel_hi:[1,0,0]
	v_pk_fma_f32 v[104:105], v[104:105], -2.0, 1.0 op_sel_hi:[1,0,0]
	ds_write_b128 v106, v[74:77]
	ds_write_b128 v106, v[78:81] offset:64
	ds_write_b128 v106, v[82:85] offset:128
	ds_write_b128 v106, v[86:89] offset:192
	ds_write_b128 v106, v[90:93] offset:256
	ds_write_b128 v106, v[94:97] offset:320
	ds_write_b128 v106, v[98:101] offset:384
	ds_write_b128 v106, v[102:105] offset:448
	ds_read_b128 v[74:77], v107
	ds_read_b128 v[78:81], v107 offset:1056
	ds_read_b128 v[82:85], v107 offset:2112
	ds_read_b128 v[86:89], v107 offset:3168
	ds_read_b128 v[90:93], v107 offset:4224
	ds_read_b128 v[94:97], v107 offset:5280
	ds_read_b128 v[98:101], v107 offset:6336
	ds_read_b128 v[102:105], v107 offset:7392
	s_waitcnt lgkmcnt(7)
	buffer_store_dwordx4 v[74:77], v132, s[8:11], 0 offen offset:512 sc0 nt sc1
	s_waitcnt lgkmcnt(6)
	buffer_store_dwordx4 v[78:81], v133, s[8:11], 0 offen offset:512 sc0 nt sc1
	s_waitcnt lgkmcnt(5)
	buffer_store_dwordx4 v[82:85], v134, s[8:11], 0 offen offset:512 sc0 nt sc1
	s_waitcnt lgkmcnt(4)
	buffer_store_dwordx4 v[86:89], v135, s[8:11], 0 offen offset:512 sc0 nt sc1
	s_waitcnt lgkmcnt(3)
	buffer_store_dwordx4 v[90:93], v136, s[8:11], 0 offen offset:512 sc0 nt sc1
	s_waitcnt lgkmcnt(2)
	buffer_store_dwordx4 v[94:97], v137, s[8:11], 0 offen offset:512 sc0 nt sc1
	s_waitcnt lgkmcnt(1)
	buffer_store_dwordx4 v[98:101], v138, s[8:11], 0 offen offset:512 sc0 nt sc1
	s_waitcnt lgkmcnt(0)
	buffer_store_dwordx4 v[102:105], v139, s[8:11], 0 offen offset:512 sc0 nt sc1
